# speedup vs baseline: 1.0277x; 1.0277x over previous
attn_fwd_pwg4x64:
	s_load_dwordx2 s[22:23], s[0:1], 0x0
	s_load_dwordx8 s[4:11], s[0:1], 0x8
	s_load_dwordx2 s[36:37], s[0:1], 0x28
	s_load_dwordx4 s[16:19], s[0:1], 0x30
	s_load_dwordx2 s[20:21], s[0:1], 0x40
	s_and_b32 s3, s2, 15
	s_bfe_u32 s30, s2, 0x30004
	s_lshr_b32 s2, s2, 3
	s_and_b32 s2, s2, 0x1ffffff0
	s_or_b32 s2, s2, s3
	s_mov_b32 s3, 0
	s_lshl_b32 s31, s30, 8
	s_lshl_b64 s[26:27], s[2:3], 19
	s_lshl_b64 s[24:25], s[2:3], 11
	s_lshl_b64 s[38:39], s[2:3], 20
	s_lshl_b32 s43, s30, 17
	s_add_u32 s38, s38, s43
	s_addc_u32 s39, s39, 0
	v_and_b32_e32 v1, 15, v0
	v_lshrrev_b32_e32 v28, 4, v0
	v_lshrrev_b32_e32 v29, 6, v0
	v_lshlrev_b32_e32 v30, 5, v1
	v_lshl_or_b32 v2, v28, 9, v30
	v_bfe_u32 v31, v0, 4, 2
	v_lshl_or_b32 v3, v31, 9, v30
	v_lshl_or_b32 v3, v29, 15, v3
	v_lshlrev_b32_e32 v32, 4, v1
	v_lshl_or_b32 v26, v28, 8, v32
	s_lshl_b32 s43, s30, 16
	v_or_b32_e32 v26, s43, v26
	v_mov_b32_e32 v208, v2
	v_lshlrev_b32_e32 v38, 2, v0
	v_lshlrev_b32_e32 v40, 14, v29
	v_lshlrev_b32_e32 v33, 12, v29
	v_mbcnt_lo_u32_b32 v204, -1, 0
	v_mbcnt_hi_u32_b32 v204, -1, v204
	v_readfirstlane_b32 s28, v33
	v_readfirstlane_b32 s29, v33
	v_mov_b32_e32 v4, 0
	v_mov_b32_e32 v5, 0
	v_mov_b32_e32 v6, 0
	v_mov_b32_e32 v7, 0
	v_mov_b32_e32 v8, 0
	v_mov_b32_e32 v9, 0
	v_mov_b32_e32 v10, 0
	v_mov_b32_e32 v11, 0
	s_mov_b32 s44, 0x3e0293ee
	s_mov_b32 s45, 0x3e0293ee
	s_waitcnt lgkmcnt(0)
	s_add_u32 s12, s4, s26
	s_addc_u32 s13, s5, s27
	s_and_b32 s13, s13, 0xffff
	s_mov_b32 s14, 0x80000
	s_mov_b32 s15, 0x20000
	s_add_u32 s4, s6, s26
	s_addc_u32 s5, s7, s27
	s_and_b32 s5, s5, 0xffff
	s_mov_b32 s6, 0x80000
	s_mov_b32 s7, 0x20000
	s_add_u32 s32, s10, s38
	s_addc_u32 s33, s11, s39
	s_add_u32 s34, s36, s38
	s_addc_u32 s35, s37, s39
	s_lshl_b32 s43, s30, 17
	s_sub_u32 s80, s34, s43
	s_subb_u32 s81, s35, 0
	s_and_b32 s81, s81, 0xffff
	s_mov_b32 s82, 0x100000
	s_mov_b32 s83, 0x20000
	s_add_i32 s86, s43, 0x8000
	s_add_u32 s40, s22, s38
	s_addc_u32 s41, s23, s39
	s_lshl_b64 s[46:47], s[2:3], 5
	s_add_u32 s10, s16, s46
	s_addc_u32 s11, s17, s47
	s_lshl_b32 s43, s30, 2
	s_add_u32 s46, s10, s43
	s_addc_u32 s47, s11, 0
	s_lshl_b64 s[26:27], s[2:3], 12
	s_add_u32 s26, s18, s26
	s_addc_u32 s27, s19, s27
	s_lshl_b32 s43, s30, 9
	s_add_u32 s26, s26, s43
	s_addc_u32 s27, s27, 0
	global_load_dwordx4 v[42:45], v2, s[32:33] nt
	global_load_dwordx4 v[46:49], v2, s[32:33] offset:16 nt
	s_add_u32 s32, s32, 8192
	s_addc_u32 s33, s33, 0
	global_load_dwordx4 v[50:53], v2, s[32:33] nt
	global_load_dwordx4 v[54:57], v2, s[32:33] offset:16 nt
	s_add_u32 s32, s32, 8192
	s_addc_u32 s33, s33, 0
	global_load_dwordx4 v[58:61], v2, s[32:33] nt
	global_load_dwordx4 v[62:65], v2, s[32:33] offset:16 nt
	s_add_u32 s32, s32, 8192
	s_addc_u32 s33, s33, 0
	global_load_dwordx4 v[66:69], v2, s[32:33] nt
	global_load_dwordx4 v[70:73], v2, s[32:33] offset:16 nt
	s_add_u32 s32, s32, 8192
	s_addc_u32 s33, s33, 0
	global_load_dwordx4 v[248:251], v2, s[32:33] nt
	global_load_dwordx4 v[252:255], v2, s[32:33] offset:16 nt
	s_add_u32 s32, s32, 8192
	s_addc_u32 s33, s33, 0
	global_load_dwordx4 v[74:77], v2, s[34:35] nt
	global_load_dwordx4 v[78:81], v2, s[34:35] offset:16 nt
	s_add_u32 s34, s34, 8192
	s_addc_u32 s35, s35, 0
	global_load_dwordx4 v[82:85], v2, s[34:35] nt
	global_load_dwordx4 v[86:89], v2, s[34:35] offset:16 nt
	s_add_u32 s34, s34, 8192
	s_addc_u32 s35, s35, 0
	global_load_dwordx4 v[90:93], v2, s[34:35] nt
	global_load_dwordx4 v[94:97], v2, s[34:35] offset:16 nt
	s_add_u32 s34, s34, 8192
	s_addc_u32 s35, s35, 0
	global_load_dwordx4 v[98:101], v2, s[34:35] nt
	global_load_dwordx4 v[102:105], v2, s[34:35] offset:16 nt
	s_add_u32 s34, s34, 8192
	s_addc_u32 s35, s35, 0
	global_load_dwordx4 v[106:109], v3, s[40:41] nt
	global_load_dwordx4 v[110:113], v3, s[40:41] offset:16 nt
	s_add_u32 s40, s40, 2048
	s_addc_u32 s41, s41, 0
	global_load_dwordx4 v[114:117], v3, s[40:41] nt
	global_load_dwordx4 v[118:121], v3, s[40:41] offset:16 nt
	s_add_u32 s40, s40, 2048
	s_addc_u32 s41, s41, 0
	global_load_dwordx4 v[122:125], v3, s[40:41] nt
	global_load_dwordx4 v[126:129], v3, s[40:41] offset:16 nt
	s_add_u32 s40, s40, 2048
	s_addc_u32 s41, s41, 0
	global_load_dwordx4 v[130:133], v3, s[40:41] nt
	global_load_dwordx4 v[134:137], v3, s[40:41] offset:16 nt
	s_add_u32 s40, s40, 2048
	s_addc_u32 s41, s41, 0
	global_load_dwordx4 v[138:141], v3, s[40:41] nt
	global_load_dwordx4 v[142:145], v3, s[40:41] offset:16 nt
	s_add_u32 s40, s40, 2048
	s_addc_u32 s41, s41, 0
	global_load_dwordx4 v[146:149], v3, s[40:41] nt
	global_load_dwordx4 v[150:153], v3, s[40:41] offset:16 nt
	s_add_u32 s40, s40, 2048
	s_addc_u32 s41, s41, 0
	global_load_dwordx4 v[154:157], v3, s[40:41] nt
	global_load_dwordx4 v[158:161], v3, s[40:41] offset:16 nt
	s_add_u32 s40, s40, 2048
	s_addc_u32 s41, s41, 0
	global_load_dwordx4 v[162:165], v3, s[40:41] nt
	global_load_dwordx4 v[166:169], v3, s[40:41] offset:16 nt
	s_add_u32 s40, s40, 2048
	s_addc_u32 s41, s41, 0
	global_load_dwordx4 v[170:173], v3, s[40:41] nt
	global_load_dwordx4 v[174:177], v3, s[40:41] offset:16 nt
	s_add_u32 s40, s40, 2048
	s_addc_u32 s41, s41, 0
	global_load_dwordx4 v[178:181], v3, s[40:41] nt
	global_load_dwordx4 v[182:185], v3, s[40:41] offset:16 nt
	s_add_u32 s40, s40, 2048
	s_addc_u32 s41, s41, 0
	global_load_dwordx4 v[186:189], v3, s[40:41] nt
	global_load_dwordx4 v[190:193], v3, s[40:41] offset:16 nt
	s_add_u32 s40, s40, 2048
	s_addc_u32 s41, s41, 0
	global_load_dwordx4 v[194:197], v3, s[40:41] nt
	global_load_dwordx4 v[198:201], v3, s[40:41] offset:16 nt
	s_add_u32 s40, s40, 2048
	s_addc_u32 s41, s41, 0
	s_waitcnt vmcnt(40)
	v_cvt_pk_bf16_f32 v12, v42, v43
	v_cvt_pk_bf16_f32 v13, v44, v45
	v_cvt_pk_bf16_f32 v14, v46, v47
	v_cvt_pk_bf16_f32 v15, v48, v49
	s_mov_b32 s42, 0x0
	buffer_store_dwordx4 v[12:15], v26, s[12:15], s42 offen sc1
	global_load_dwordx4 v[42:45], v3, s[40:41] nt
	global_load_dwordx4 v[46:49], v3, s[40:41] offset:16 nt
	s_add_u32 s40, s40, 2048
	s_addc_u32 s41, s41, 0
	s_waitcnt vmcnt(41)
	v_cvt_pk_bf16_f32 v16, v50, v51
	v_cvt_pk_bf16_f32 v17, v52, v53
	v_cvt_pk_bf16_f32 v18, v54, v55
	v_cvt_pk_bf16_f32 v19, v56, v57
	s_mov_b32 s42, 0x1000
	buffer_store_dwordx4 v[16:19], v26, s[12:15], s42 offen sc1
	global_load_dwordx4 v[50:53], v3, s[40:41] nt
	global_load_dwordx4 v[54:57], v3, s[40:41] offset:16 nt
	s_add_u32 s40, s40, 2048
	s_addc_u32 s41, s41, 0
	s_waitcnt vmcnt(42)
	v_cvt_pk_bf16_f32 v20, v58, v59
	v_cvt_pk_bf16_f32 v21, v60, v61
	v_cvt_pk_bf16_f32 v22, v62, v63
	v_cvt_pk_bf16_f32 v23, v64, v65
	s_mov_b32 s42, 0x2000
	buffer_store_dwordx4 v[20:23], v26, s[12:15], s42 offen sc1
	global_load_dwordx4 v[58:61], v3, s[40:41] nt
	global_load_dwordx4 v[62:65], v3, s[40:41] offset:16 nt
	s_add_u32 s40, s40, 2048
	s_addc_u32 s41, s41, 0
	s_waitcnt vmcnt(43)
	v_cvt_pk_bf16_f32 v12, v66, v67
	v_cvt_pk_bf16_f32 v13, v68, v69
	v_cvt_pk_bf16_f32 v14, v70, v71
	v_cvt_pk_bf16_f32 v15, v72, v73
	s_mov_b32 s42, 0x3000
	buffer_store_dwordx4 v[12:15], v26, s[12:15], s42 offen sc1
	global_load_dwordx4 v[66:69], v3, s[40:41] nt
	global_load_dwordx4 v[70:73], v3, s[40:41] offset:16 nt
	s_add_u32 s40, s40, 2048
	s_addc_u32 s41, s41, 0
	s_waitcnt vmcnt(42)
	v_mov_b32_e32 v4, 0
	v_mov_b32_e32 v5, 0
	v_mov_b32_e32 v6, 0
	v_mov_b32_e32 v7, 0
	v_mov_b32_e32 v8, 0
	v_mov_b32_e32 v9, 0
	v_mov_b32_e32 v10, 0
	v_mov_b32_e32 v11, 0
	v_pk_add_f32 v[4:5], v[74:75], v[4:5]
	v_pk_add_f32 v[6:7], v[76:77], v[6:7]
	v_pk_add_f32 v[8:9], v[78:79], v[8:9]
	v_pk_add_f32 v[10:11], v[80:81], v[10:11]
	v_cvt_pk_bf16_f32 v16, v74, v75
	v_cvt_pk_bf16_f32 v17, v76, v77
	v_cvt_pk_bf16_f32 v18, v78, v79
	v_cvt_pk_bf16_f32 v19, v80, v81
	s_mov_b32 s42, 0x0
	buffer_store_dwordx4 v[16:19], v26, s[4:7], s42 offen sc1
	s_waitcnt vmcnt(41)
	v_pk_add_f32 v[4:5], v[82:83], v[4:5]
	v_pk_add_f32 v[6:7], v[84:85], v[6:7]
	v_pk_add_f32 v[8:9], v[86:87], v[8:9]
	v_pk_add_f32 v[10:11], v[88:89], v[10:11]
	v_cvt_pk_bf16_f32 v20, v82, v83
	v_cvt_pk_bf16_f32 v21, v84, v85
	v_cvt_pk_bf16_f32 v22, v86, v87
	v_cvt_pk_bf16_f32 v23, v88, v89
	s_mov_b32 s42, 0x1000
	buffer_store_dwordx4 v[20:23], v26, s[4:7], s42 offen sc1
	s_waitcnt vmcnt(40)
	v_pk_add_f32 v[4:5], v[90:91], v[4:5]
	v_pk_add_f32 v[6:7], v[92:93], v[6:7]
	v_pk_add_f32 v[8:9], v[94:95], v[8:9]
	v_pk_add_f32 v[10:11], v[96:97], v[10:11]
	v_cvt_pk_bf16_f32 v12, v90, v91
	v_cvt_pk_bf16_f32 v13, v92, v93
	v_cvt_pk_bf16_f32 v14, v94, v95
	v_cvt_pk_bf16_f32 v15, v96, v97
	s_mov_b32 s42, 0x2000
	buffer_store_dwordx4 v[12:15], v26, s[4:7], s42 offen sc1
	s_waitcnt vmcnt(39)
	v_pk_add_f32 v[4:5], v[98:99], v[4:5]
	v_pk_add_f32 v[6:7], v[100:101], v[6:7]
	v_pk_add_f32 v[8:9], v[102:103], v[8:9]
	v_pk_add_f32 v[10:11], v[104:105], v[10:11]
	v_cvt_pk_bf16_f32 v16, v98, v99
	v_cvt_pk_bf16_f32 v17, v100, v101
	v_cvt_pk_bf16_f32 v18, v102, v103
	v_cvt_pk_bf16_f32 v19, v104, v105
	s_mov_b32 s42, 0x3000
	buffer_store_dwordx4 v[16:19], v26, s[4:7], s42 offen sc1
	s_movk_i32 s0, 0x80
	v_cmp_gt_u32_e64 s[0:1], s0, v0
	s_waitcnt vmcnt(0)
	s_barrier
	v_cmp_eq_u32_e32 vcc, 0, v0
	s_and_saveexec_b64 s[38:39], vcc
	s_cbranch_execz .Lpro_noflag
	v_mov_b32_e32 v12, 0x600df1a6
	v_mov_b32_e32 v13, 0
	global_store_dword v13, v12, s[46:47] sc1
.Lpro_noflag:
	s_or_b64 exec, exec, s[38:39]
	v_lshlrev_b32_e32 v41, 2, v204
	v_and_b32_e32 v41, 28, v41
	global_load_dword v30, v41, s[10:11] sc1
	v_lshrrev_b32_e32 v202, 4, v204
	v_and_b32_e32 v31, 15, v204
	v_xor_b32_e32 v32, v31, v202
	v_xor_b32_e32 v33, 4, v32
	v_lshlrev_b32_e32 v34, 8, v202
	v_or_b32_e32 v35, 0x10000, v40
	v_add_u32_e32 v34, v34, v35
	v_lshl_add_u32 v24, v32, 4, v34
	v_lshl_add_u32 v25, v33, 4, v34
	v_pk_mul_f32 v[106:107], v[106:107], s[44:45] op_sel_hi:[1,0]
	v_pk_mul_f32 v[108:109], v[108:109], s[44:45] op_sel_hi:[1,0]
	v_pk_mul_f32 v[110:111], v[110:111], s[44:45] op_sel_hi:[1,0]
	v_pk_mul_f32 v[112:113], v[112:113], s[44:45] op_sel_hi:[1,0]
	v_cvt_pk_bf16_f32 v12, v106, v107
	v_cvt_pk_bf16_f32 v13, v108, v109
	v_cvt_pk_bf16_f32 v14, v110, v111
	v_cvt_pk_bf16_f32 v15, v112, v113
	ds_write_b128 v24, v[12:15] offset:0
	v_pk_mul_f32 v[114:115], v[114:115], s[44:45] op_sel_hi:[1,0]
	v_pk_mul_f32 v[116:117], v[116:117], s[44:45] op_sel_hi:[1,0]
	v_pk_mul_f32 v[118:119], v[118:119], s[44:45] op_sel_hi:[1,0]
	v_pk_mul_f32 v[120:121], v[120:121], s[44:45] op_sel_hi:[1,0]
	v_cvt_pk_bf16_f32 v16, v114, v115
	v_cvt_pk_bf16_f32 v17, v116, v117
	v_cvt_pk_bf16_f32 v18, v118, v119
	v_cvt_pk_bf16_f32 v19, v120, v121
	ds_write_b128 v25, v[16:19] offset:1024
	v_pk_mul_f32 v[122:123], v[122:123], s[44:45] op_sel_hi:[1,0]
	v_pk_mul_f32 v[124:125], v[124:125], s[44:45] op_sel_hi:[1,0]
	v_pk_mul_f32 v[126:127], v[126:127], s[44:45] op_sel_hi:[1,0]
	v_pk_mul_f32 v[128:129], v[128:129], s[44:45] op_sel_hi:[1,0]
	v_cvt_pk_bf16_f32 v20, v122, v123
	v_cvt_pk_bf16_f32 v21, v124, v125
	v_cvt_pk_bf16_f32 v22, v126, v127
	v_cvt_pk_bf16_f32 v23, v128, v129
	ds_write_b128 v24, v[20:23] offset:2048
	v_pk_mul_f32 v[130:131], v[130:131], s[44:45] op_sel_hi:[1,0]
	v_pk_mul_f32 v[132:133], v[132:133], s[44:45] op_sel_hi:[1,0]
	v_pk_mul_f32 v[134:135], v[134:135], s[44:45] op_sel_hi:[1,0]
	v_pk_mul_f32 v[136:137], v[136:137], s[44:45] op_sel_hi:[1,0]
	v_cvt_pk_bf16_f32 v12, v130, v131
	v_cvt_pk_bf16_f32 v13, v132, v133
	v_cvt_pk_bf16_f32 v14, v134, v135
	v_cvt_pk_bf16_f32 v15, v136, v137
	ds_write_b128 v25, v[12:15] offset:3072
	v_pk_mul_f32 v[138:139], v[138:139], s[44:45] op_sel_hi:[1,0]
	v_pk_mul_f32 v[140:141], v[140:141], s[44:45] op_sel_hi:[1,0]
	v_pk_mul_f32 v[142:143], v[142:143], s[44:45] op_sel_hi:[1,0]
	v_pk_mul_f32 v[144:145], v[144:145], s[44:45] op_sel_hi:[1,0]
	v_cvt_pk_bf16_f32 v16, v138, v139
	v_cvt_pk_bf16_f32 v17, v140, v141
	v_cvt_pk_bf16_f32 v18, v142, v143
	v_cvt_pk_bf16_f32 v19, v144, v145
	ds_write_b128 v24, v[16:19] offset:4096
	v_pk_mul_f32 v[146:147], v[146:147], s[44:45] op_sel_hi:[1,0]
	v_pk_mul_f32 v[148:149], v[148:149], s[44:45] op_sel_hi:[1,0]
	v_pk_mul_f32 v[150:151], v[150:151], s[44:45] op_sel_hi:[1,0]
	v_pk_mul_f32 v[152:153], v[152:153], s[44:45] op_sel_hi:[1,0]
	v_cvt_pk_bf16_f32 v20, v146, v147
	v_cvt_pk_bf16_f32 v21, v148, v149
	v_cvt_pk_bf16_f32 v22, v150, v151
	v_cvt_pk_bf16_f32 v23, v152, v153
	ds_write_b128 v25, v[20:23] offset:5120
	v_pk_mul_f32 v[154:155], v[154:155], s[44:45] op_sel_hi:[1,0]
	v_pk_mul_f32 v[156:157], v[156:157], s[44:45] op_sel_hi:[1,0]
	v_pk_mul_f32 v[158:159], v[158:159], s[44:45] op_sel_hi:[1,0]
	v_pk_mul_f32 v[160:161], v[160:161], s[44:45] op_sel_hi:[1,0]
	v_cvt_pk_bf16_f32 v12, v154, v155
	v_cvt_pk_bf16_f32 v13, v156, v157
	v_cvt_pk_bf16_f32 v14, v158, v159
	v_cvt_pk_bf16_f32 v15, v160, v161
	ds_write_b128 v24, v[12:15] offset:6144
	v_pk_mul_f32 v[162:163], v[162:163], s[44:45] op_sel_hi:[1,0]
	v_pk_mul_f32 v[164:165], v[164:165], s[44:45] op_sel_hi:[1,0]
	v_pk_mul_f32 v[166:167], v[166:167], s[44:45] op_sel_hi:[1,0]
	v_pk_mul_f32 v[168:169], v[168:169], s[44:45] op_sel_hi:[1,0]
	v_cvt_pk_bf16_f32 v16, v162, v163
	v_cvt_pk_bf16_f32 v17, v164, v165
	v_cvt_pk_bf16_f32 v18, v166, v167
	v_cvt_pk_bf16_f32 v19, v168, v169
	ds_write_b128 v25, v[16:19] offset:7168
	v_pk_mul_f32 v[170:171], v[170:171], s[44:45] op_sel_hi:[1,0]
	v_pk_mul_f32 v[172:173], v[172:173], s[44:45] op_sel_hi:[1,0]
	v_pk_mul_f32 v[174:175], v[174:175], s[44:45] op_sel_hi:[1,0]
	v_pk_mul_f32 v[176:177], v[176:177], s[44:45] op_sel_hi:[1,0]
	v_cvt_pk_bf16_f32 v20, v170, v171
	v_cvt_pk_bf16_f32 v21, v172, v173
	v_cvt_pk_bf16_f32 v22, v174, v175
	v_cvt_pk_bf16_f32 v23, v176, v177
	ds_write_b128 v24, v[20:23] offset:8192
	v_pk_mul_f32 v[178:179], v[178:179], s[44:45] op_sel_hi:[1,0]
	v_pk_mul_f32 v[180:181], v[180:181], s[44:45] op_sel_hi:[1,0]
	v_pk_mul_f32 v[182:183], v[182:183], s[44:45] op_sel_hi:[1,0]
	v_pk_mul_f32 v[184:185], v[184:185], s[44:45] op_sel_hi:[1,0]
	v_cvt_pk_bf16_f32 v12, v178, v179
	v_cvt_pk_bf16_f32 v13, v180, v181
	v_cvt_pk_bf16_f32 v14, v182, v183
	v_cvt_pk_bf16_f32 v15, v184, v185
	ds_write_b128 v25, v[12:15] offset:9216
	v_pk_mul_f32 v[186:187], v[186:187], s[44:45] op_sel_hi:[1,0]
	v_pk_mul_f32 v[188:189], v[188:189], s[44:45] op_sel_hi:[1,0]
	v_pk_mul_f32 v[190:191], v[190:191], s[44:45] op_sel_hi:[1,0]
	v_pk_mul_f32 v[192:193], v[192:193], s[44:45] op_sel_hi:[1,0]
	v_cvt_pk_bf16_f32 v16, v186, v187
	v_cvt_pk_bf16_f32 v17, v188, v189
	v_cvt_pk_bf16_f32 v18, v190, v191
	v_cvt_pk_bf16_f32 v19, v192, v193
	ds_write_b128 v24, v[16:19] offset:10240
	v_pk_mul_f32 v[194:195], v[194:195], s[44:45] op_sel_hi:[1,0]
	v_pk_mul_f32 v[196:197], v[196:197], s[44:45] op_sel_hi:[1,0]
	v_pk_mul_f32 v[198:199], v[198:199], s[44:45] op_sel_hi:[1,0]
	v_pk_mul_f32 v[200:201], v[200:201], s[44:45] op_sel_hi:[1,0]
	v_cvt_pk_bf16_f32 v20, v194, v195
	v_cvt_pk_bf16_f32 v21, v196, v197
	v_cvt_pk_bf16_f32 v22, v198, v199
	v_cvt_pk_bf16_f32 v23, v200, v201
	ds_write_b128 v25, v[20:23] offset:11264
	v_pk_mul_f32 v[42:43], v[42:43], s[44:45] op_sel_hi:[1,0]
	v_pk_mul_f32 v[44:45], v[44:45], s[44:45] op_sel_hi:[1,0]
	v_pk_mul_f32 v[46:47], v[46:47], s[44:45] op_sel_hi:[1,0]
	v_pk_mul_f32 v[48:49], v[48:49], s[44:45] op_sel_hi:[1,0]
	v_cvt_pk_bf16_f32 v12, v42, v43
	v_cvt_pk_bf16_f32 v13, v44, v45
	v_cvt_pk_bf16_f32 v14, v46, v47
	v_cvt_pk_bf16_f32 v15, v48, v49
	ds_write_b128 v24, v[12:15] offset:12288
	v_pk_mul_f32 v[50:51], v[50:51], s[44:45] op_sel_hi:[1,0]
	v_pk_mul_f32 v[52:53], v[52:53], s[44:45] op_sel_hi:[1,0]
	v_pk_mul_f32 v[54:55], v[54:55], s[44:45] op_sel_hi:[1,0]
	v_pk_mul_f32 v[56:57], v[56:57], s[44:45] op_sel_hi:[1,0]
	v_cvt_pk_bf16_f32 v16, v50, v51
	v_cvt_pk_bf16_f32 v17, v52, v53
	v_cvt_pk_bf16_f32 v18, v54, v55
	v_cvt_pk_bf16_f32 v19, v56, v57
	ds_write_b128 v25, v[16:19] offset:13312
	v_pk_mul_f32 v[58:59], v[58:59], s[44:45] op_sel_hi:[1,0]
	v_pk_mul_f32 v[60:61], v[60:61], s[44:45] op_sel_hi:[1,0]
	v_pk_mul_f32 v[62:63], v[62:63], s[44:45] op_sel_hi:[1,0]
	v_pk_mul_f32 v[64:65], v[64:65], s[44:45] op_sel_hi:[1,0]
	v_cvt_pk_bf16_f32 v20, v58, v59
	v_cvt_pk_bf16_f32 v21, v60, v61
	v_cvt_pk_bf16_f32 v22, v62, v63
	v_cvt_pk_bf16_f32 v23, v64, v65
	ds_write_b128 v24, v[20:23] offset:14336
	v_pk_mul_f32 v[66:67], v[66:67], s[44:45] op_sel_hi:[1,0]
	v_pk_mul_f32 v[68:69], v[68:69], s[44:45] op_sel_hi:[1,0]
	v_pk_mul_f32 v[70:71], v[70:71], s[44:45] op_sel_hi:[1,0]
	v_pk_mul_f32 v[72:73], v[72:73], s[44:45] op_sel_hi:[1,0]
	v_cvt_pk_bf16_f32 v12, v66, v67
	v_cvt_pk_bf16_f32 v13, v68, v69
	v_cvt_pk_bf16_f32 v14, v70, v71
	v_cvt_pk_bf16_f32 v15, v72, v73
	ds_write_b128 v25, v[12:15] offset:15360
	v_mov_b32_e32 v209, v41
	v_lshrrev_b32_e32 v29, 6, v0
	s_nop 0
	v_readfirstlane_b32 s50, v29
	s_mov_b32 s51, s30
	s_add_i32 s52, s24, s31
	s_mov_b32 s54, s32
	s_mov_b32 s55, s33
	s_lshl_b32 s43, s30, 16
	s_add_i32 s56, s43, 0x4000
	s_add_u32 s74, s34, 0x10000
	s_addc_u32 s75, s35, 0
	s_mov_b32 s76, s26
	s_mov_b32 s77, s27
	v_mov_b32_e32 v200, v4
	v_mov_b32_e32 v201, v5
	v_mov_b32_e32 v202, v6
	v_mov_b32_e32 v203, v7
	v_mov_b32_e32 v204, v8
	v_mov_b32_e32 v205, v9
	v_mov_b32_e32 v206, v10
	v_mov_b32_e32 v207, v11
	s_add_i32 s61, s28, s43
	s_add_i32 s43, s30, 1
	s_and_b32 s43, s43, 7
	s_lshl_b32 s43, s43, 16
	s_add_i32 s62, s28, s43
	s_add_i32 s43, s30, 2
	s_and_b32 s43, s43, 7
	s_lshl_b32 s43, s43, 16
	s_add_i32 s63, s28, s43
	s_add_i32 s43, s30, 3
	s_and_b32 s43, s43, 7
	s_lshl_b32 s43, s43, 16
	s_add_i32 s87, s28, s43
	s_add_i32 s43, s30, 7
	s_and_b32 s43, s43, 7
	s_lshl_b32 s43, s43, 16
	s_add_i32 s88, s28, s43
	s_add_i32 s88, s88, 0xc000
	s_mov_b32 s58, s87
	s_mov_b32 s57, s63
	s_mov_b32 s59, 0x10000
	s_mov_b32 s60, 0x10000
	s_lshl_b32 s43, s50, 11
	s_add_i32 s84, s43, 0x24000
	s_add_i32 s85, s84, 0x3f0
	s_mov_b32 s64, s10
	s_mov_b32 s65, s11
	s_mov_b32 s66, 0x10000
	s_mov_b32 s67, 0x4000
	s_mov_b32 s68, 0xc000
	s_mov_b32 s69, 0x14000
	s_mov_b32 s70, 0x600df1a6
	s_mov_b32 s71, 0x155510
	s_mov_b32 s72, s46
	s_mov_b32 s73, s47
	s_mov_b32 m0, s84
	s_nop 0
	buffer_load_dwordx4 v208, s[80:83], s86 offen lds
	s_mov_b32 m0, s85
	s_nop 0
	buffer_load_dwordx4 v208, s[80:83], s86 offen offset:16 lds
	s_add_i32 s86, s86, 0x2000
	s_mov_b32 s22, 0x600df1a6
	s_mov_b32 s23, 0x10000
	s_waitcnt vmcnt(0) lgkmcnt(0)
	v_cmp_eq_u32_e32 vcc, s22, v30
	s_cmp_eq_u64 vcc, exec
	s_cbranch_scc0 .LBB0_27
.LBB0_11:
	v_bfe_u32 v3, v0, 5, 1
	v_lshlrev_b32_e32 v4, 8, v0
	v_and_b32_e32 v4, 0x1f00, v4
	v_and_b32_e32 v5, 7, v0
	v_bitop3_b32 v6, v3, v0, 7 bitop3:0x78
	v_lshl_or_b32 v64, v6, 4, v4
	v_bitop3_b32 v6, v3, v5, 2 bitop3:0x36
	v_lshl_or_b32 v65, v6, 4, v4
	v_bitop3_b32 v6, v3, v5, 4 bitop3:0x36
	v_bitop3_b32 v5, v3, v5, 6 bitop3:0x36
	v_lshl_or_b32 v66, v6, 4, v4
	v_lshl_or_b32 v67, v5, 4, v4
	v_and_b32_e32 v4, 3, v0
	v_lshlrev_b32_e32 v6, 4, v0
	v_lshlrev_b32_e32 v5, 3, v4
	v_and_b32_e32 v6, 0xc0, v6
	v_lshlrev_b32_e32 v8, 1, v0
	v_lshlrev_b32_e32 v9, 8, v3
	v_bfe_u32 v7, v0, 4, 2
	v_and_b32_e32 v8, 32, v8
	v_or3_b32 v5, v5, v9, v6
	s_mov_b32 s0, 0x8000
	v_or3_b32 v184, v5, v8, s0
	v_lshlrev_b32_e32 v5, 8, v7
	v_xor_b32_e32 v6, v7, v1
	s_cmp_lg_u32 0, -1
	v_lshl_or_b32 v222, v6, 4, v5
	v_bitop3_b32 v1, v7, v1, 4 bitop3:0x36
	s_mov_b32 m0, s29
	s_nop 0
	buffer_load_dwordx4 v222, s[12:15], s61 offen lds
	s_cselect_b32 s17, 0, 0
	v_lshl_or_b32 v223, v1, 4, v5
	s_add_i32 s20, s29, 0x400
	s_add_i32 s0, s61, 0x400
	s_mov_b32 m0, s20
	s_nop 0
	buffer_load_dwordx4 v223, s[12:15], s0 offen lds
	v_lshlrev_b32_e32 v0, 6, v0
	s_add_i32 s21, s29, 0x800
	s_add_i32 s0, s61, 0x800
	s_mov_b32 m0, s21
	s_nop 0
	buffer_load_dwordx4 v222, s[12:15], s0 offen lds
	v_and_b32_e32 v0, 0x700, v0
	v_lshlrev_b32_e32 v1, 6, v3
	v_lshlrev_b32_e32 v3, 4, v4
	s_add_i32 s22, s29, 0xc00
	s_add_i32 s1, s61, 0xc00
	s_mov_b32 m0, s22
	s_nop 0
	buffer_load_dwordx4 v223, s[12:15], s1 offen lds
	v_or3_b32 v196, v0, v1, v3
	s_add_i32 s2, s29, 0x8000
	s_mov_b32 m0, s2
	s_nop 0
	buffer_load_dwordx4 v196, s[4:7], s61 offen lds
	s_add_i32 s1, s2, 0x400
	s_add_i32 s3, s61, 0x80
	s_mov_b32 m0, s1
	s_nop 0
	buffer_load_dwordx4 v196, s[4:7], s3 offen lds
	s_add_i32 s1, s2, 0x800
	s_mov_b32 m0, s1
	s_nop 0
	buffer_load_dwordx4 v196, s[4:7], s0 offen lds
	s_add_i32 s0, s2, 0xc00
	s_add_i32 s1, s61, 0x880
	s_mov_b32 m0, s0
	s_nop 0
	buffer_load_dwordx4 v196, s[4:7], s1 offen lds
	s_add_i32 s3, s29, 0x4000
	s_add_i32 s19, s62, 0x0
	s_mov_b32 m0, s3
	s_nop 0
	buffer_load_dwordx4 v222, s[12:15], s19 offen lds
	v_or_b32_e32 v2, 0x10000, v40
	v_add_u32_e32 v218, s17, v64
	v_add_u32_e32 v219, s17, v65
	v_add_u32_e32 v220, s17, v66
	v_add_u32_e32 v221, s17, v67
	s_add_i32 s10, s29, 0x4400
	s_add_i32 s0, s62, 0x400
	s_mov_b32 m0, s10
	s_nop 0
	buffer_load_dwordx4 v223, s[12:15], s0 offen lds
	s_add_i32 s11, s29, 0x4800
	s_add_i32 s18, s62, 0x800
	s_mov_b32 m0, s11
	s_nop 0
	buffer_load_dwordx4 v222, s[12:15], s18 offen lds
	v_add_u32_e32 v32, v2, v218
	v_add_u32_e32 v33, v2, v219
	v_add_u32_e32 v34, v2, v220
	v_add_u32_e32 v35, v2, v221
	s_add_i32 s16, s29, 0x4c00
	s_add_i32 s0, s62, 0xc00
	s_mov_b32 m0, s16
	s_nop 0
	buffer_load_dwordx4 v223, s[12:15], s0 offen lds
	v_add_u32_e32 v212, s17, v184
	ds_read_b128 v[0:3], v32 offset:0
	ds_read_b128 v[4:7], v33 offset:0
	ds_read_b128 v[8:11], v34 offset:0
	ds_read_b128 v[12:15], v35 offset:0
	ds_read_b128 v[16:19], v32 offset:128
	ds_read_b128 v[20:23], v33 offset:128
	ds_read_b128 v[24:27], v34 offset:128
	ds_read_b128 v[28:31], v35 offset:128
	s_waitcnt lgkmcnt(0)
	v_accvgpr_write_b32 a[128], v0
	v_accvgpr_write_b32 a[129], v1
	v_accvgpr_write_b32 a[130], v2
	v_accvgpr_write_b32 a[131], v3
	v_accvgpr_write_b32 a[132], v4
	v_accvgpr_write_b32 a[133], v5
	v_accvgpr_write_b32 a[134], v6
	v_accvgpr_write_b32 a[135], v7
	v_accvgpr_write_b32 a[136], v8
	v_accvgpr_write_b32 a[137], v9
	v_accvgpr_write_b32 a[138], v10
	v_accvgpr_write_b32 a[139], v11
	v_accvgpr_write_b32 a[140], v12
	v_accvgpr_write_b32 a[141], v13
	v_accvgpr_write_b32 a[142], v14
	v_accvgpr_write_b32 a[143], v15
	v_accvgpr_write_b32 a[144], v16
	v_accvgpr_write_b32 a[145], v17
	v_accvgpr_write_b32 a[146], v18
	v_accvgpr_write_b32 a[147], v19
	v_accvgpr_write_b32 a[148], v20
	v_accvgpr_write_b32 a[149], v21
	v_accvgpr_write_b32 a[150], v22
	v_accvgpr_write_b32 a[151], v23
	v_accvgpr_write_b32 a[152], v24
	v_accvgpr_write_b32 a[153], v25
	v_accvgpr_write_b32 a[154], v26
	v_accvgpr_write_b32 a[155], v27
	v_accvgpr_write_b32 a[156], v28
	v_accvgpr_write_b32 a[157], v29
	v_accvgpr_write_b32 a[158], v30
	v_accvgpr_write_b32 a[159], v31
	ds_read_b128 v[0:3], v32 offset:8192
	ds_read_b128 v[4:7], v33 offset:8192
	ds_read_b128 v[8:11], v34 offset:8192
	ds_read_b128 v[12:15], v35 offset:8192
	ds_read_b128 v[16:19], v32 offset:8320
	ds_read_b128 v[20:23], v33 offset:8320
	ds_read_b128 v[24:27], v34 offset:8320
	ds_read_b128 v[28:31], v35 offset:8320
	s_waitcnt lgkmcnt(0)
	v_accvgpr_write_b32 a[160], v0
	v_accvgpr_write_b32 a[161], v1
	v_accvgpr_write_b32 a[162], v2
	v_accvgpr_write_b32 a[163], v3
	v_accvgpr_write_b32 a[164], v4
	v_accvgpr_write_b32 a[165], v5
	v_accvgpr_write_b32 a[166], v6
	v_accvgpr_write_b32 a[167], v7
	v_accvgpr_write_b32 a[168], v8
	v_accvgpr_write_b32 a[169], v9
	v_accvgpr_write_b32 a[170], v10
	v_accvgpr_write_b32 a[171], v11
	v_accvgpr_write_b32 a[172], v12
	v_accvgpr_write_b32 a[173], v13
	v_accvgpr_write_b32 a[174], v14
	v_accvgpr_write_b32 a[175], v15
	v_accvgpr_write_b32 a[176], v16
	v_accvgpr_write_b32 a[177], v17
	v_accvgpr_write_b32 a[178], v18
	v_accvgpr_write_b32 a[179], v19
	v_accvgpr_write_b32 a[180], v20
	v_accvgpr_write_b32 a[181], v21
	v_accvgpr_write_b32 a[182], v22
	v_accvgpr_write_b32 a[183], v23
	v_accvgpr_write_b32 a[184], v24
	v_accvgpr_write_b32 a[185], v25
	v_accvgpr_write_b32 a[186], v26
	v_accvgpr_write_b32 a[187], v27
	v_accvgpr_write_b32 a[188], v28
	v_accvgpr_write_b32 a[189], v29
	v_accvgpr_write_b32 a[190], v30
	v_accvgpr_write_b32 a[191], v31
	s_waitcnt vmcnt(0) lgkmcnt(0)
	s_barrier
	s_nop 0
	ds_read_b128 a[192:195], v218 offset:0
	s_nop 0
	ds_read_b128 a[196:199], v219 offset:0
	ds_read_b128 a[200:203], v220 offset:0
	ds_read_b128 a[204:207], v221 offset:0
	ds_read_b128 a[208:211], v218 offset:128
	ds_read_b128 a[212:215], v219 offset:128
	ds_read_b128 a[216:219], v220 offset:128
	ds_read_b128 a[220:223], v221 offset:128
	ds_read_b128 a[224:227], v218 offset:8192
	ds_read_b128 a[228:231], v219 offset:8192
	ds_read_b128 a[232:235], v220 offset:8192
	ds_read_b128 a[236:239], v221 offset:8192
	ds_read_b128 a[240:243], v218 offset:8320
	ds_read_b128 a[244:247], v219 offset:8320
	ds_read_b128 a[248:251], v220 offset:8320
	ds_read_b128 a[252:255], v221 offset:8320
	s_waitcnt lgkmcnt(0)
	v_mfma_f32_32x32x16_bf16 v[48:63], a[192:195], a[128:131], 0
	v_mfma_f32_32x32x16_bf16 v[32:47], a[192:195], a[160:163], 0
	v_mfma_f32_32x32x16_bf16 v[0:15], a[224:227], a[128:131], 0
	v_mfma_f32_32x32x16_bf16 v[16:31], a[224:227], a[160:163], 0
	v_mfma_f32_32x32x16_bf16 v[48:63], a[196:199], a[132:135], v[48:63]
	v_mfma_f32_32x32x16_bf16 v[32:47], a[196:199], a[164:167], v[32:47]
	v_mfma_f32_32x32x16_bf16 v[0:15], a[228:231], a[132:135], v[0:15]
	v_mfma_f32_32x32x16_bf16 v[16:31], a[228:231], a[164:167], v[16:31]
	v_mfma_f32_32x32x16_bf16 v[48:63], a[200:203], a[136:139], v[48:63]
	v_mfma_f32_32x32x16_bf16 v[32:47], a[200:203], a[168:171], v[32:47]
	v_mfma_f32_32x32x16_bf16 v[0:15], a[232:235], a[136:139], v[0:15]
	v_mfma_f32_32x32x16_bf16 v[16:31], a[232:235], a[168:171], v[16:31]
	v_mfma_f32_32x32x16_bf16 v[48:63], a[204:207], a[140:143], v[48:63]
	v_mfma_f32_32x32x16_bf16 v[32:47], a[204:207], a[172:175], v[32:47]
	v_mfma_f32_32x32x16_bf16 v[0:15], a[236:239], a[140:143], v[0:15]
	v_mfma_f32_32x32x16_bf16 v[16:31], a[236:239], a[172:175], v[16:31]
	v_mfma_f32_32x32x16_bf16 v[48:63], a[208:211], a[144:147], v[48:63]
	s_mov_b32 s27, s29
	v_mfma_f32_32x32x16_bf16 v[32:47], a[208:211], a[176:179], v[32:47]
	s_add_i32 s0, s63, 0x0
	s_mov_b32 s30, s0
	v_mfma_f32_32x32x16_bf16 v[0:15], a[240:243], a[144:147], v[0:15]
	s_mov_b32 s31, s20
	v_mfma_f32_32x32x16_bf16 v[16:31], a[240:243], a[176:179], v[16:31]
	s_add_i32 s33, s63, 0x400
	v_mfma_f32_32x32x16_bf16 v[48:63], a[212:215], a[148:151], v[48:63]
	s_mov_b32 s34, s21
	v_mfma_f32_32x32x16_bf16 v[32:47], a[212:215], a[180:183], v[32:47]
	s_add_i32 s1, s63, 0x800
	s_mov_b32 s35, s1
	v_mfma_f32_32x32x16_bf16 v[0:15], a[244:247], a[148:151], v[0:15]
	s_mov_b32 s36, s22
	v_mfma_f32_32x32x16_bf16 v[16:31], a[244:247], a[180:183], v[16:31]
	s_add_i32 s37, s63, 0xc00
	v_mfma_f32_32x32x16_bf16 v[48:63], a[216:219], a[152:155], v[48:63]
	s_add_i32 s23, s29, 0xc000
	s_mov_b32 s38, s23
	v_mfma_f32_32x32x16_bf16 v[32:47], a[216:219], a[184:187], v[32:47]
	v_mfma_f32_32x32x16_bf16 v[0:15], a[248:251], a[152:155], v[0:15]
	s_add_i32 s24, s29, 0xc400
	s_mov_b32 s39, s24
	v_mfma_f32_32x32x16_bf16 v[16:31], a[248:251], a[184:187], v[16:31]
	s_add_i32 s40, s62, 0x80
	v_mfma_f32_32x32x16_bf16 v[48:63], a[220:223], a[156:159], v[48:63]
	s_add_i32 s25, s29, 0xc800
	s_mov_b32 s41, s25
	v_mfma_f32_32x32x16_bf16 v[32:47], a[220:223], a[188:191], v[32:47]
	v_mfma_f32_32x32x16_bf16 v[0:15], a[252:255], a[156:159], v[0:15]
	s_add_i32 s26, s29, 0xcc00
	s_mov_b32 s42, s26
	v_mfma_f32_32x32x16_bf16 v[16:31], a[252:255], a[188:191], v[16:31]
	s_add_i32 s43, s62, 0x880
	s_waitcnt vmcnt(0) lgkmcnt(0)
	s_barrier
	s_nop 0
	s_mov_b32 m0, s27
	s_nop 0
	buffer_load_dwordx4 v222, s[12:15], s30 offen lds
	s_mov_b32 m0, s31
	s_nop 0
	buffer_load_dwordx4 v223, s[12:15], s33 offen lds
	s_addk_i32 s17, 0x4000
	v_add_u32_e32 v217, s17, v64
	ds_read_b128 a[192:195], v217 offset:0
	s_mov_b32 m0, s34
	s_nop 0
	buffer_load_dwordx4 v222, s[12:15], s35 offen lds
	v_add_u32_e32 v199, s17, v65
	ds_read_b128 a[196:199], v199 offset:0
	s_mov_b32 m0, s36
	s_nop 0
	buffer_load_dwordx4 v223, s[12:15], s37 offen lds
	v_add_u32_e32 v198, s17, v66
	ds_read_b128 a[200:203], v198 offset:0
	s_mov_b32 m0, s38
	s_nop 0
	buffer_load_dwordx4 v196, s[4:7], s19 offen lds
	v_add_u32_e32 v197, s17, v67
	ds_read_b128 a[204:207], v197 offset:0
	s_mov_b32 m0, s39
	s_nop 0
	buffer_load_dwordx4 v196, s[4:7], s40 offen lds
	ds_read_b128 a[208:211], v217 offset:128
	s_mov_b32 m0, s41
	s_nop 0
	buffer_load_dwordx4 v196, s[4:7], s18 offen lds
	ds_read_b128 a[212:215], v199 offset:128
	s_mov_b32 m0, s42
	s_nop 0
	buffer_load_dwordx4 v196, s[4:7], s43 offen lds
	ds_read_b128 a[216:219], v198 offset:128
	ds_read_b128 a[220:223], v197 offset:128
	v_cvt_pk_bf16_f32 v248, v248, v249
	v_cvt_pk_bf16_f32 v249, v250, v251
	v_cvt_pk_bf16_f32 v250, v252, v253
	v_cvt_pk_bf16_f32 v251, v254, v255
	v_lshrrev_b32_e32 v252, 1, v208
	buffer_store_dwordx4 v[248:251], v252, s[12:15], s56 offen sc1
	v_mbcnt_lo_u32_b32 v253, -1, 0
	v_mbcnt_hi_u32_b32 v253, -1, v253
	v_lshlrev_b32_e32 v253, 4, v253
	v_add_u32_e32 v253, s84, v253
	ds_read_b128 v[248:251], v253
	ds_read_b128 v[252:255], v253 offset:1024
	v_max3_f32 v64, v48, v49, v0
	v_max3_f32 v65, v50, v51, v1
	v_max3_f32 v64, v64, v2, v3
	ds_read_b128 a[224:227], v217 offset:8192
	v_max3_f32 v64, v64, v52, v53
	v_max3_f32 v65, v65, v54, v55
	v_max3_f32 v64, v64, v4, v5
	v_max3_f32 v65, v65, v6, v7
	ds_read_b128 a[228:231], v199 offset:8192
	v_max3_f32 v64, v64, v56, v57
	v_max3_f32 v65, v65, v58, v59
	v_max3_f32 v64, v64, v8, v9
	v_max3_f32 v65, v65, v10, v11
	ds_read_b128 a[232:235], v198 offset:8192
	v_max3_f32 v64, v64, v60, v61
	v_max3_f32 v65, v65, v62, v63
	v_max3_f32 v64, v64, v12, v13
	v_max3_f32 v65, v65, v14, v15
	ds_read_b128 a[236:239], v197 offset:8192
	v_max3_f32 v66, v32, v33, v16
	v_max3_f32 v67, v34, v35, v17
	v_max3_f32 v66, v66, v18, v19
	ds_read_b128 a[240:243], v217 offset:8320
	v_max3_f32 v66, v66, v36, v37
	v_max3_f32 v67, v67, v38, v39
	v_max3_f32 v66, v66, v20, v21
	v_max3_f32 v67, v67, v22, v23
	ds_read_b128 a[244:247], v199 offset:8320
	v_max3_f32 v66, v66, v40, v41
	v_max3_f32 v67, v67, v42, v43
	v_max3_f32 v66, v66, v24, v25
	v_max3_f32 v67, v67, v26, v27
	ds_read_b128 a[248:251], v198 offset:8320
	v_max3_f32 v66, v66, v44, v45
	v_max3_f32 v67, v67, v46, v47
	v_max3_f32 v66, v66, v28, v29
	v_max3_f32 v67, v67, v30, v31
	ds_read_b128 a[252:255], v197 offset:8320
	s_waitcnt lgkmcnt(8)
	v_pk_add_f32 v[200:201], v[248:249], v[200:201]
	v_pk_add_f32 v[202:203], v[250:251], v[202:203]
	v_pk_add_f32 v[204:205], v[252:253], v[204:205]
	v_pk_add_f32 v[206:207], v[254:255], v[206:207]
	v_cvt_pk_bf16_f32 v248, v248, v249
	v_cvt_pk_bf16_f32 v249, v250, v251
	v_cvt_pk_bf16_f32 v250, v252, v253
	v_cvt_pk_bf16_f32 v251, v254, v255
	v_lshrrev_b32_e32 v252, 1, v208
	buffer_store_dwordx4 v[248:251], v252, s[4:7], s56 offen sc1
	s_add_i32 s56, s56, 0x1000
	s_nop 1
	global_load_dwordx4 v[248:251], v208, s[54:55] nt
	global_load_dwordx4 v[252:255], v208, s[54:55] offset:16 nt
	s_add_u32 s54, s54, 0x2000
	s_addc_u32 s55, s55, 0
	s_mov_b32 m0, s84
	s_nop 0
	buffer_load_dwordx4 v208, s[80:83], s86 offen lds
	s_mov_b32 m0, s85
	s_nop 0
	buffer_load_dwordx4 v208, s[80:83], s86 offen offset:16 lds
	s_add_i32 s86, s86, 0x2000
	v_max_f32_e32 v64, v64, v65
	v_mov_b32_e32 v65, v64
	s_nop 1
	v_permlane32_swap_b32_e32 v64, v65
	v_max_f32_e32 v214, v64, v65
	v_max_f32_e32 v64, v66, v67
	v_mov_b32_e32 v65, v64
	s_nop 1
	v_permlane32_swap_b32_e32 v64, v65
	v_max_f32_e32 v213, v64, v65
	v_sub_f32_e32 v64, v0, v214
	v_mbcnt_lo_u32_b32 v0, -1, 0
	v_mbcnt_hi_u32_b32 v0, -1, v0
	v_sub_f32_e32 v65, v1, v214
	v_xor_b32_e32 v1, 0x80000000, v214
	v_cmp_gt_u32_e32 vcc, 32, v0
	v_sub_f32_e32 v128, v2, v214
	v_sub_f32_e32 v129, v3, v214
	v_sub_f32_e32 v130, v4, v214
	v_sub_f32_e32 v131, v5, v214
	v_sub_f32_e32 v132, v6, v214
	v_sub_f32_e32 v133, v7, v214
	v_sub_f32_e32 v134, v8, v214
	v_sub_f32_e32 v135, v9, v214
	v_sub_f32_e32 v136, v10, v214
	v_sub_f32_e32 v137, v11, v214
	v_sub_f32_e32 v138, v12, v214
	v_sub_f32_e32 v139, v13, v214
	v_sub_f32_e32 v140, v14, v214
	v_sub_f32_e32 v141, v15, v214
	v_sub_f32_e32 v142, v16, v213
	v_mov_b32_e32 v211, 1.0
	v_sub_f32_e32 v143, v17, v213
	v_xor_b32_e32 v17, 0x80000000, v213
	v_cndmask_b32_e64 v0, 0, 1.0, vcc
	s_nop 1
	v_mfma_f32_32x32x2_f32 v[0:15], v0, v1, 0
	v_mbcnt_lo_u32_b32 v16, -1, 0
	v_mbcnt_hi_u32_b32 v16, -1, v16
	v_sub_f32_e32 v48, v48, v214
	v_sub_f32_e32 v49, v49, v214
	v_sub_f32_e32 v50, v50, v214
	v_sub_f32_e32 v51, v51, v214
	v_sub_f32_e32 v52, v52, v214
	v_sub_f32_e32 v53, v53, v214
	v_sub_f32_e32 v54, v54, v214
	v_sub_f32_e32 v55, v55, v214
	v_sub_f32_e32 v56, v56, v214
	v_sub_f32_e32 v57, v57, v214
	v_sub_f32_e32 v58, v58, v214
	v_sub_f32_e32 v59, v59, v214
	v_sub_f32_e32 v60, v60, v214
	v_sub_f32_e32 v61, v61, v214
	v_sub_f32_e32 v62, v62, v214
	v_sub_f32_e32 v63, v63, v214
	v_sub_f32_e32 v32, v32, v213
	v_sub_f32_e32 v33, v33, v213
	v_sub_f32_e32 v34, v34, v213
	v_cmp_gt_u32_e32 vcc, 32, v16
	v_sub_f32_e32 v35, v35, v213
	v_sub_f32_e32 v36, v36, v213
	v_sub_f32_e32 v37, v37, v213
	v_sub_f32_e32 v38, v38, v213
	v_sub_f32_e32 v39, v39, v213
	v_sub_f32_e32 v40, v40, v213
	v_sub_f32_e32 v41, v41, v213
	v_sub_f32_e32 v42, v42, v213
	v_sub_f32_e32 v43, v43, v213
	v_sub_f32_e32 v44, v44, v213
	v_sub_f32_e32 v45, v45, v213
	v_sub_f32_e32 v46, v46, v213
	v_sub_f32_e32 v47, v47, v213
	v_sub_f32_e32 v144, v18, v213
	v_sub_f32_e32 v145, v19, v213
	v_sub_f32_e32 v146, v20, v213
	v_sub_f32_e32 v147, v21, v213
	v_sub_f32_e32 v183, v22, v213
	v_sub_f32_e32 v194, v23, v213
	v_cndmask_b32_e64 v16, 0, 1.0, vcc
	v_sub_f32_e32 v195, v24, v213
	v_sub_f32_e32 v215, v25, v213
	v_sub_f32_e32 v216, v26, v213
	v_sub_f32_e32 v224, v27, v213
	v_sub_f32_e32 v225, v28, v213
	v_sub_f32_e32 v226, v29, v213
	v_sub_f32_e32 v229, v30, v213
	v_sub_f32_e32 v230, v31, v213
	v_mfma_f32_32x32x2_f32 v[16:31], v16, v17, 0
	v_exp_f32_e32 v112, v48
	v_exp_f32_e32 v113, v49
	v_exp_f32_e32 v114, v50
	v_exp_f32_e32 v115, v51
	v_mov_b32_e32 v193, 0
	v_add_f32_e32 v48, v193, v112
	v_add_f32_e32 v49, v193, v113
	v_exp_f32_e32 v116, v52
	v_exp_f32_e32 v117, v53
	v_exp_f32_e32 v118, v54
	v_add_f32_e32 v48, v48, v114
	v_add_f32_e32 v49, v49, v115
	v_exp_f32_e32 v119, v55
	v_exp_f32_e32 v120, v56
	v_add_f32_e32 v48, v48, v116
	v_add_f32_e32 v49, v49, v117
	v_add_f32_e32 v48, v48, v118
	v_exp_f32_e32 v121, v57
	v_exp_f32_e32 v122, v58
	v_exp_f32_e32 v123, v59
	v_add_f32_e32 v49, v49, v119
	v_add_f32_e32 v48, v48, v120
	v_exp_f32_e32 v124, v60
	v_exp_f32_e32 v125, v61
	v_add_f32_e32 v49, v49, v121
	v_add_f32_e32 v48, v48, v122
	v_add_f32_e32 v49, v49, v123
	v_exp_f32_e32 v126, v62
	v_exp_f32_e32 v127, v63
	v_exp_f32_e32 v96, v32
	v_add_f32_e32 v32, v48, v124
	v_add_f32_e32 v48, v49, v125
	v_exp_f32_e32 v97, v33
	v_exp_f32_e32 v98, v34
	v_add_f32_e32 v231, v32, v126
	v_add_f32_e32 v232, v48, v127
	v_add_f32_e32 v32, v193, v96
	v_exp_f32_e32 v99, v35
	v_exp_f32_e32 v100, v36
	v_exp_f32_e32 v101, v37
	v_add_f32_e32 v33, v193, v97
	v_add_f32_e32 v32, v32, v98
	v_exp_f32_e32 v102, v38
	v_exp_f32_e32 v103, v39
	v_add_f32_e32 v33, v33, v99
	v_add_f32_e32 v32, v32, v100
	v_add_f32_e32 v33, v33, v101
	v_exp_f32_e32 v104, v40
	v_exp_f32_e32 v105, v41
	v_exp_f32_e32 v106, v42
	v_add_f32_e32 v32, v32, v102
	v_add_f32_e32 v33, v33, v103
	v_exp_f32_e32 v107, v43
	v_exp_f32_e32 v108, v44
	v_add_f32_e32 v32, v32, v104
	v_add_f32_e32 v33, v33, v105
	v_add_f32_e32 v32, v32, v106
	v_exp_f32_e32 v109, v45
	v_exp_f32_e32 v110, v46
	v_exp_f32_e32 v111, v47
	v_add_f32_e32 v33, v33, v107
	v_add_f32_e32 v32, v32, v108
	s_waitcnt lgkmcnt(0)
	v_add_f32_e32 v33, v33, v109
	v_add_f32_e32 v233, v32, v110
	v_add_f32_e32 v234, v33, v111
	v_mfma_f32_32x32x16_bf16 v[80:95], a[192:195], a[128:131], v[0:15]
	ds_read_b64_tr_b16 v[160:161], v212 offset:0
	v_exp_f32_e32 v235, v64
	v_exp_f32_e32 v236, v65
	v_cvt_pk_bf16_f32 v152, v112, v113
	v_mfma_f32_32x32x16_bf16 v[64:79], a[192:195], a[160:163], v[16:31]
	ds_read_b64_tr_b16 v[162:163], v212 offset:0x800
	v_exp_f32_e32 v237, v128
	v_exp_f32_e32 v238, v129
	v_cvt_pk_bf16_f32 v153, v114, v115
	v_exp_f32_e32 v115, v130
	v_mfma_f32_32x32x16_bf16 v[48:63], a[224:227], a[128:131], v[0:15]
	ds_read_b64_tr_b16 v[172:173], v212 offset:0x200
	v_exp_f32_e32 v239, v131
	v_cvt_pk_bf16_f32 v154, v116, v117
	v_mfma_f32_32x32x16_bf16 v[32:47], a[224:227], a[160:163], v[16:31]
	ds_read_b64_tr_b16 v[174:175], v212 offset:0xa00
	ds_read_b64_tr_b16 v[168:169], v212 offset:0x400
	v_exp_f32_e32 v240, v132
	v_exp_f32_e32 v241, v133
	v_cvt_pk_bf16_f32 v155, v118, v119
	v_exp_f32_e32 v185, v134
	v_exp_f32_e32 v186, v135
	v_mfma_f32_32x32x16_bf16 v[80:95], a[196:199], a[132:135], v[80:95]
	ds_read_b64_tr_b16 v[170:171], v212 offset:0xc00
	v_cvt_pk_bf16_f32 v128, v120, v121
	v_exp_f32_e32 v187, v136
	v_exp_f32_e32 v188, v137
	v_mfma_f32_32x32x16_bf16 v[64:79], a[196:199], a[164:167], v[64:79]
	ds_read_b64_tr_b16 v[176:177], v212 offset:0x600
	v_cvt_pk_bf16_f32 v129, v122, v123
	v_exp_f32_e32 v189, v138
	v_exp_f32_e32 v190, v139
	v_mfma_f32_32x32x16_bf16 v[48:63], a[228:231], a[132:135], v[48:63]
	ds_read_b64_tr_b16 v[178:179], v212 offset:0xe00
	v_cvt_pk_bf16_f32 v130, v124, v125
	v_mfma_f32_32x32x16_bf16 v[32:47], a[228:231], a[164:167], v[32:47]
	ds_read_b64_tr_b16 v[164:165], v212 offset:0x1000
	v_exp_f32_e32 v191, v140
	v_exp_f32_e32 v192, v141
	ds_read_b64_tr_b16 v[166:167], v212 offset:0x1800
	v_cvt_pk_bf16_f32 v131, v126, v127
	v_exp_f32_e32 v141, v142
	v_exp_f32_e32 v142, v143
	v_mfma_f32_32x32x16_bf16 v[80:95], a[200:203], a[136:139], v[80:95]
	ds_read_b64_tr_b16 v[156:157], v212 offset:0x1200
	v_cvt_pk_bf16_f32 v180, v96, v97
	v_exp_f32_e32 v143, v144
	v_mfma_f32_32x32x16_bf16 v[64:79], a[200:203], a[168:171], v[64:79]
	ds_read_b64_tr_b16 v[158:159], v212 offset:0x1a00
	v_exp_f32_e32 v242, v145
	v_cvt_pk_bf16_f32 v181, v98, v99
	v_mfma_f32_32x32x16_bf16 v[48:63], a[232:235], a[136:139], v[48:63]
	ds_read_b64_tr_b16 v[148:149], v212 offset:0x1400
	v_exp_f32_e32 v243, v146
	v_exp_f32_e32 v244, v147
	v_cvt_pk_bf16_f32 v182, v100, v101
	v_mfma_f32_32x32x16_bf16 v[32:47], a[232:235], a[168:171], v[32:47]
	ds_read_b64_tr_b16 v[150:151], v212 offset:0x1c00
	ds_read_b64_tr_b16 v[136:137], v212 offset:0x1600
	v_exp_f32_e32 v245, v183
	v_exp_f32_e32 v246, v194
	v_cvt_pk_bf16_f32 v183, v102, v103
	v_exp_f32_e32 v194, v195
	v_exp_f32_e32 v195, v215
	v_mfma_f32_32x32x16_bf16 v[80:95], a[204:207], a[140:143], v[80:95]
	ds_read_b64_tr_b16 v[138:139], v212 offset:0x1e00
	v_cvt_pk_bf16_f32 v144, v104, v105
	v_exp_f32_e32 v215, v216
	v_exp_f32_e32 v224, v224
	v_mfma_f32_32x32x16_bf16 v[64:79], a[204:207], a[172:175], v[64:79]
	ds_read_b64_tr_b16 v[132:133], v212 offset:0x2000
	v_cvt_pk_bf16_f32 v145, v106, v107
	v_exp_f32_e32 v227, v225
	v_exp_f32_e32 v228, v226
	v_mfma_f32_32x32x16_bf16 v[48:63], a[236:239], a[140:143], v[48:63]
	ds_read_b64_tr_b16 v[134:135], v212 offset:0x2800
	v_cvt_pk_bf16_f32 v146, v108, v109
	v_mfma_f32_32x32x16_bf16 v[32:47], a[236:239], a[172:175], v[32:47]
	ds_read_b64_tr_b16 v[124:125], v212 offset:0x2200
	v_exp_f32_e32 v229, v229
	v_exp_f32_e32 v230, v230
	ds_read_b64_tr_b16 v[126:127], v212 offset:0x2a00
	v_cvt_pk_bf16_f32 v147, v110, v111
	s_mov_b32 s27, s3
	v_mfma_f32_32x32x16_bf16 v[80:95], a[208:211], a[144:147], v[80:95]
	ds_read_b64_tr_b16 v[120:121], v212 offset:0x2400
	v_cvt_pk_bf16_f32 v112, v235, v236
	v_add_f32_e32 v96, v231, v235
	v_add_f32_e32 v97, v232, v236
	s_add_i32 s30, s87, 0x0
	v_mfma_f32_32x32x16_bf16 v[64:79], a[208:211], a[176:179], v[64:79]
	ds_read_b64_tr_b16 v[122:123], v212 offset:0x2c00
	v_cvt_pk_bf16_f32 v113, v237, v238
	v_add_f32_e32 v96, v96, v237
	v_add_f32_e32 v97, v97, v238
	s_mov_b32 s31, s10
	v_mfma_f32_32x32x16_bf16 v[48:63], a[240:243], a[144:147], v[48:63]
	ds_read_b64_tr_b16 v[116:117], v212 offset:0x2600
	v_cvt_pk_bf16_f32 v114, v115, v239
	v_add_f32_e32 v96, v96, v115
	v_add_f32_e32 v97, v97, v239
	s_add_i32 s33, s87, 0x400
	v_mfma_f32_32x32x16_bf16 v[32:47], a[240:243], a[176:179], v[32:47]
	ds_read_b64_tr_b16 v[118:119], v212 offset:0x2e00
	ds_read_b64_tr_b16 v[104:105], v212 offset:0x3000
	v_cvt_pk_bf16_f32 v115, v240, v241
	v_add_f32_e32 v96, v96, v240
	v_add_f32_e32 v97, v97, v241
	s_mov_b32 s34, s11
	v_mfma_f32_32x32x16_bf16 v[80:95], a[212:215], a[148:151], v[80:95]
	ds_read_b64_tr_b16 v[106:107], v212 offset:0x3800
	v_add_f32_e32 v96, v96, v185
	v_add_f32_e32 v97, v97, v186
	s_add_i32 s35, s87, 0x800
	v_mfma_f32_32x32x16_bf16 v[64:79], a[212:215], a[180:183], v[64:79]
	ds_read_b64_tr_b16 v[108:109], v212 offset:0x3200
	v_add_f32_e32 v96, v96, v187
	v_add_f32_e32 v97, v97, v188
	s_mov_b32 s36, s16
	v_mfma_f32_32x32x16_bf16 v[48:63], a[244:247], a[148:151], v[48:63]
	ds_read_b64_tr_b16 v[110:111], v212 offset:0x3a00
	v_add_f32_e32 v96, v96, v189
	v_add_f32_e32 v97, v97, v190
	s_add_i32 s37, s87, 0xc00
	v_mfma_f32_32x32x16_bf16 v[32:47], a[244:247], a[180:183], v[32:47]
	ds_read_b64_tr_b16 v[100:101], v212 offset:0x3400
	ds_read_b64_tr_b16 v[102:103], v212 offset:0x3c00
	v_add_f32_e32 v216, v96, v191
	v_add_f32_e32 v225, v97, v192
	s_mov_b32 s38, s2
	v_mfma_f32_32x32x16_bf16 v[80:95], a[216:219], a[152:155], v[80:95]
	ds_read_b64_tr_b16 v[96:97], v212 offset:0x3600
	v_cvt_pk_bf16_f32 v140, v141, v142
	v_add_f32_e32 v226, v233, v141
	v_add_f32_e32 v142, v234, v142
	v_mfma_f32_32x32x16_bf16 v[64:79], a[216:219], a[184:187], v[64:79]
	ds_read_b64_tr_b16 v[98:99], v212 offset:0x3e00
	v_cvt_pk_bf16_f32 v141, v143, v242
	v_add_f32_e32 v143, v226, v143
	v_add_f32_e32 v226, v142, v242
	v_mfma_f32_32x32x16_bf16 v[48:63], a[248:251], a[152:155], v[48:63]
	s_add_i32 s17, s29, 0x8400
	s_mov_b32 s39, s17
	v_cvt_pk_bf16_f32 v142, v243, v244
	v_add_f32_e32 v231, v143, v243
	v_add_f32_e32 v226, v226, v244
	v_mfma_f32_32x32x16_bf16 v[32:47], a[248:251], a[184:187], v[32:47]
	s_add_i32 s40, s63, 0x80
	v_cvt_pk_bf16_f32 v143, v245, v246
	v_add_f32_e32 v231, v231, v245
	v_add_f32_e32 v226, v226, v246
	v_mfma_f32_32x32x16_bf16 v[80:95], a[220:223], a[156:159], v[80:95]
	s_add_i32 s18, s29, 0x8800
	s_mov_b32 s41, s18
	v_add_f32_e32 v231, v231, v194
	v_add_f32_e32 v226, v226, v195
	v_mfma_f32_32x32x16_bf16 v[64:79], a[220:223], a[188:191], v[64:79]
	v_add_f32_e32 v231, v231, v215
	v_add_f32_e32 v226, v226, v224
	v_mfma_f32_32x32x16_bf16 v[48:63], a[252:255], a[156:159], v[48:63]
	s_add_i32 s19, s29, 0x8c00
	s_mov_b32 s42, s19
	v_add_f32_e32 v231, v231, v227
	v_add_f32_e32 v226, v226, v228
	v_mfma_f32_32x32x16_bf16 v[32:47], a[252:255], a[188:191], v[32:47]
	s_add_i32 s43, s63, 0x880
	v_add_f32_e32 v231, v231, v229
	v_add_f32_e32 v226, v226, v230
	v_add_f32_e32 v216, v216, v225
	s_waitcnt vmcnt(0) lgkmcnt(0)
	s_barrier
	v_mfma_f32_32x32x16_bf16 a[0:15], v[160:163], v[152:155], 0
	v_mov_b32_e32 v225, v216
	s_mov_b32 m0, s27
	s_nop 0
	buffer_load_dwordx4 v222, s[12:15], s30 offen lds
	v_mfma_f32_32x32x16_bf16 a[16:31], v[160:163], v[180:183], 0
	v_permlane32_swap_b32_e32 v216, v225
	v_add_f32_e32 v216, v216, v225
	s_mov_b32 m0, s31
	s_nop 0
	buffer_load_dwordx4 v223, s[12:15], s33 offen lds
	ds_read_b128 a[192:195], v218 offset:0
	v_mfma_f32_32x32x16_bf16 a[32:47], v[172:175], v[152:155], 0
	v_add_f32_e32 v225, v193, v216
	v_add_f32_e32 v216, v231, v226
	v_mov_b32_e32 v226, v216
	s_mov_b32 m0, s34
	s_nop 0
	buffer_load_dwordx4 v222, s[12:15], s35 offen lds
	ds_read_b128 a[196:199], v219 offset:0
	v_mfma_f32_32x32x16_bf16 a[48:63], v[172:175], v[180:183], 0
	v_permlane32_swap_b32_e32 v216, v226
	v_add_f32_e32 v216, v216, v226
	s_mov_b32 m0, s36
	s_nop 0
	buffer_load_dwordx4 v223, s[12:15], s37 offen lds
	ds_read_b128 a[200:203], v220 offset:0
	v_mfma_f32_32x32x16_bf16 a[64:79], v[168:171], v[152:155], 0
	v_add_f32_e32 v226, v193, v216
	s_mov_b32 m0, s38
	s_nop 0
	buffer_load_dwordx4 v196, s[4:7], s0 offen lds
	ds_read_b128 a[204:207], v221 offset:0
	v_mfma_f32_32x32x16_bf16 a[80:95], v[168:171], v[180:183], 0
	s_mov_b32 m0, s39
	s_nop 0
	buffer_load_dwordx4 v196, s[4:7], s40 offen lds
	ds_read_b128 a[208:211], v218 offset:128
	v_mfma_f32_32x32x16_bf16 a[96:111], v[176:179], v[152:155], 0
	s_mov_b32 m0, s41
	s_nop 0
	buffer_load_dwordx4 v196, s[4:7], s1 offen lds
	ds_read_b128 a[212:215], v219 offset:128
	v_mfma_f32_32x32x16_bf16 a[112:127], v[176:179], v[180:183], 0
	s_mov_b32 m0, s42
	s_nop 0
	buffer_load_dwordx4 v196, s[4:7], s43 offen lds
	ds_read_b128 a[216:219], v220 offset:128
	v_mfma_f32_32x32x16_bf16 a[0:15], v[164:167], v[128:131], a[0:15]
	ds_read_b128 a[220:223], v221 offset:128
	v_cvt_pk_bf16_f32 v248, v248, v249
	v_cvt_pk_bf16_f32 v249, v250, v251
	v_cvt_pk_bf16_f32 v250, v252, v253
	v_cvt_pk_bf16_f32 v251, v254, v255
	v_lshrrev_b32_e32 v252, 1, v208
	buffer_store_dwordx4 v[248:251], v252, s[12:15], s56 offen sc1
	v_mbcnt_lo_u32_b32 v253, -1, 0
	v_mbcnt_hi_u32_b32 v253, -1, v253
	v_lshlrev_b32_e32 v253, 4, v253
	v_add_u32_e32 v253, s84, v253
	ds_read_b128 v[248:251], v253
	ds_read_b128 v[252:255], v253 offset:1024
	v_max3_f32 v152, v80, v81, v48
	v_max3_f32 v153, v82, v83, v49
	v_max3_f32 v152, v152, v50, v51
	v_mfma_f32_32x32x16_bf16 a[16:31], v[164:167], v[144:147], a[16:31]
	ds_read_b128 a[224:227], v218 offset:8192
	v_max3_f32 v152, v152, v84, v85
	v_max3_f32 v153, v153, v86, v87
	v_max3_f32 v152, v152, v52, v53
	v_max3_f32 v153, v153, v54, v55
	v_mfma_f32_32x32x16_bf16 a[32:47], v[156:159], v[128:131], a[32:47]
	ds_read_b128 a[228:231], v219 offset:8192
	v_max3_f32 v152, v152, v88, v89
	v_max3_f32 v153, v153, v90, v91
	v_max3_f32 v152, v152, v56, v57
	v_max3_f32 v153, v153, v58, v59
	v_mfma_f32_32x32x16_bf16 a[48:63], v[156:159], v[144:147], a[48:63]
	ds_read_b128 a[232:235], v220 offset:8192
	v_max3_f32 v152, v152, v92, v93
	v_max3_f32 v153, v153, v94, v95
	v_max3_f32 v152, v152, v60, v61
	v_max3_f32 v153, v153, v62, v63
	v_mfma_f32_32x32x16_bf16 a[64:79], v[148:151], v[128:131], a[64:79]
	ds_read_b128 a[236:239], v221 offset:8192
	v_max3_f32 v154, v64, v65, v32
	v_max3_f32 v155, v66, v67, v33
	v_max3_f32 v154, v154, v34, v35
	v_mfma_f32_32x32x16_bf16 a[80:95], v[148:151], v[144:147], a[80:95]
	ds_read_b128 a[240:243], v218 offset:8320
	v_max3_f32 v148, v154, v68, v69
	v_max3_f32 v149, v155, v70, v71
	v_max3_f32 v148, v148, v36, v37
	v_max3_f32 v149, v149, v38, v39
	v_mfma_f32_32x32x16_bf16 a[96:111], v[136:139], v[128:131], a[96:111]
	ds_read_b128 a[244:247], v219 offset:8320
	v_max3_f32 v128, v148, v72, v73
	v_max3_f32 v129, v149, v74, v75
	v_max3_f32 v128, v128, v40, v41
	v_max3_f32 v129, v129, v42, v43
	v_mfma_f32_32x32x16_bf16 a[112:127], v[136:139], v[144:147], a[112:127]
	ds_read_b128 a[248:251], v220 offset:8320
	v_max3_f32 v128, v128, v76, v77
	v_max3_f32 v129, v129, v78, v79
	v_max3_f32 v128, v128, v44, v45
	v_max3_f32 v130, v129, v46, v47
	v_mfma_f32_32x32x16_bf16 a[0:15], v[132:135], v[112:115], a[0:15]
	ds_read_b128 a[252:255], v221 offset:8320
	s_waitcnt lgkmcnt(8)
	v_pk_add_f32 v[200:201], v[248:249], v[200:201]
	v_pk_add_f32 v[202:203], v[250:251], v[202:203]
	v_pk_add_f32 v[204:205], v[252:253], v[204:205]
	v_pk_add_f32 v[206:207], v[254:255], v[206:207]
	v_cvt_pk_bf16_f32 v248, v248, v249
	v_cvt_pk_bf16_f32 v249, v250, v251
	v_cvt_pk_bf16_f32 v250, v252, v253
	v_cvt_pk_bf16_f32 v251, v254, v255
	v_lshrrev_b32_e32 v252, 1, v208
	buffer_store_dwordx4 v[248:251], v252, s[4:7], s56 offen sc1
	s_add_i32 s56, s56, 0x1000
	s_nop 1
	global_load_dwordx4 v[248:251], v208, s[54:55] nt
	global_load_dwordx4 v[252:255], v208, s[54:55] offset:16 nt
	s_add_u32 s54, s54, 0x2000
	s_addc_u32 s55, s55, 0
	s_mov_b32 m0, s84
	s_nop 0
	buffer_load_dwordx4 v208, s[80:83], s86 offen lds
	s_mov_b32 m0, s85
	s_nop 0
	buffer_load_dwordx4 v208, s[80:83], s86 offen offset:16 lds
	s_add_i32 s86, s86, 0x2000
	v_max_f32_e32 v129, v152, v153
	v_mov_b32_e32 v131, v129
	s_nop 1
	v_permlane32_swap_b32_e32 v129, v131
	v_max_f32_e32 v129, v129, v131
	v_mfma_f32_32x32x16_bf16 a[16:31], v[132:135], v[140:143], a[16:31]
	v_max_f32_e32 v128, v128, v130
	v_mov_b32_e32 v130, v128
	s_nop 1
	v_permlane32_swap_b32_e32 v128, v130
	v_max_f32_e32 v128, v128, v130
	v_max_f32_e32 v130, v129, v129
	v_max_f32_e32 v131, v128, v128
	v_max_f32_e32 v130, v130, v131
	s_mov_b32 s0, 0x41000000
	v_mfma_f32_32x32x16_bf16 a[32:47], v[124:127], v[112:115], a[32:47]
	v_cmp_lt_f32_e32 vcc, s0, v130
	s_cmp_lg_u64 vcc, 0
	s_cselect_b64 s[0:1], -1, 0
	s_cbranch_vccnz .LBB0_41
	v_mov_b32_e32 v216, 1.0

.LBB0_17:
	v_mfma_f32_32x32x16_bf16 v[112:127], a[192:195], a[128:131], v[0:15]
	v_exp_f32_e32 v48, v48
	v_exp_f32_e32 v49, v49
	ds_read_b64_tr_b16 v[172:173], v215 offset:0
	v_cvt_pk_bf16_f32 v164, v128, v129
	v_exp_f32_e32 v50, v50
	v_exp_f32_e32 v51, v51
	v_mfma_f32_32x32x16_bf16 v[96:111], a[192:195], a[160:163], v[16:31]
	ds_read_b64_tr_b16 v[174:175], v215 offset:0x800
	v_cvt_pk_bf16_f32 v165, v130, v131
	v_mfma_f32_32x32x16_bf16 v[80:95], a[224:227], a[128:131], v[0:15]
	ds_read_b64_tr_b16 v[184:185], v215 offset:0x200
	v_exp_f32_e32 v239, v52
	v_exp_f32_e32 v240, v53
	v_cvt_pk_bf16_f32 v166, v132, v133
	v_mfma_f32_32x32x16_bf16 v[64:79], a[224:227], a[160:163], v[16:31]
	ds_read_b64_tr_b16 v[186:187], v215 offset:0xa00
	ds_read_b64_tr_b16 v[180:181], v215 offset:0x400
	v_exp_f32_e32 v241, v54
	v_exp_f32_e32 v242, v55
	v_cvt_pk_bf16_f32 v167, v134, v135
	v_exp_f32_e32 v227, v56
	v_exp_f32_e32 v228, v57
	v_mfma_f32_32x32x16_bf16 v[112:127], a[196:199], a[132:135], v[112:127]
	ds_read_b64_tr_b16 v[182:183], v215 offset:0xc00
	v_cvt_pk_bf16_f32 v128, v136, v137
	v_exp_f32_e32 v229, v58
	v_exp_f32_e32 v230, v59
	v_mfma_f32_32x32x16_bf16 v[96:111], a[196:199], a[164:167], v[96:111]
	ds_read_b64_tr_b16 v[188:189], v215 offset:0x600
	v_cvt_pk_bf16_f32 v129, v138, v139
	v_exp_f32_e32 v231, v60
	v_exp_f32_e32 v232, v61
	v_mfma_f32_32x32x16_bf16 v[80:95], a[228:231], a[132:135], v[80:95]
	ds_read_b64_tr_b16 v[190:191], v215 offset:0xe00
	v_cvt_pk_bf16_f32 v130, v140, v141
	v_mfma_f32_32x32x16_bf16 v[64:79], a[228:231], a[164:167], v[64:79]
	ds_read_b64_tr_b16 v[176:177], v215 offset:0x1000
	v_exp_f32_e32 v233, v62
	v_exp_f32_e32 v234, v63
	ds_read_b64_tr_b16 v[178:179], v215 offset:0x1800
	v_cvt_pk_bf16_f32 v131, v142, v143
	v_exp_f32_e32 v141, v32
	v_exp_f32_e32 v142, v33
	v_mfma_f32_32x32x16_bf16 v[112:127], a[200:203], a[136:139], v[112:127]
	ds_read_b64_tr_b16 v[168:169], v215 offset:0x1200
	v_cvt_pk_bf16_f32 v192, v144, v145
	v_exp_f32_e32 v143, v34
	v_mfma_f32_32x32x16_bf16 v[96:111], a[200:203], a[168:171], v[96:111]
	ds_read_b64_tr_b16 v[170:171], v215 offset:0x1a00
	v_exp_f32_e32 v243, v35
	v_cvt_pk_bf16_f32 v193, v146, v147
	v_mfma_f32_32x32x16_bf16 v[80:95], a[232:235], a[136:139], v[80:95]
	ds_read_b64_tr_b16 v[160:161], v215 offset:0x1400
	v_exp_f32_e32 v244, v36
	v_exp_f32_e32 v245, v37
	v_cvt_pk_bf16_f32 v194, v148, v149
	v_mfma_f32_32x32x16_bf16 v[64:79], a[232:235], a[168:171], v[64:79]
	ds_read_b64_tr_b16 v[162:163], v215 offset:0x1c00
	ds_read_b64_tr_b16 v[136:137], v215 offset:0x1600
	v_exp_f32_e32 v246, v38
	v_exp_f32_e32 v247, v39
	v_cvt_pk_bf16_f32 v195, v150, v151
	v_exp_f32_e32 v148, v40
	v_exp_f32_e32 v149, v41
	v_mfma_f32_32x32x16_bf16 v[112:127], a[204:207], a[140:143], v[112:127]
	ds_read_b64_tr_b16 v[138:139], v215 offset:0x1e00
	v_cvt_pk_bf16_f32 v144, v152, v153
	v_exp_f32_e32 v150, v42
	v_exp_f32_e32 v151, v43
	v_mfma_f32_32x32x16_bf16 v[96:111], a[204:207], a[172:175], v[96:111]
	ds_read_b64_tr_b16 v[132:133], v215 offset:0x2000
	v_cvt_pk_bf16_f32 v145, v154, v155
	v_exp_f32_e32 v152, v44
	v_exp_f32_e32 v153, v45
	v_mfma_f32_32x32x16_bf16 v[80:95], a[236:239], a[140:143], v[80:95]
	ds_read_b64_tr_b16 v[134:135], v215 offset:0x2800
	v_cvt_pk_bf16_f32 v146, v156, v157
	v_mfma_f32_32x32x16_bf16 v[64:79], a[236:239], a[172:175], v[64:79]
	ds_read_b64_tr_b16 v[60:61], v215 offset:0x2200
	v_exp_f32_e32 v154, v46
	v_exp_f32_e32 v155, v47
	ds_read_b64_tr_b16 v[62:63], v215 offset:0x2a00
	v_cvt_pk_bf16_f32 v147, v158, v159
	s_mov_b32 s0, s29
	v_mfma_f32_32x32x16_bf16 v[112:127], a[208:211], a[144:147], v[112:127]
	ds_read_b64_tr_b16 v[56:57], v215 offset:0x2400
	v_cvt_pk_bf16_f32 v52, v48, v49
	v_add_f32_e32 v32, v236, v48
	v_add_f32_e32 v33, v235, v49
	s_add_i32 s57, s58, s59
	s_and_b32 s57, s57, 0x7ffff
	s_mov_b32 s33, s57
	s_mov_b32 s1, s33
	v_mfma_f32_32x32x16_bf16 v[96:111], a[208:211], a[176:179], v[96:111]
	ds_read_b64_tr_b16 v[58:59], v215 offset:0x2c00
	v_cvt_pk_bf16_f32 v53, v50, v51
	v_add_f32_e32 v32, v32, v50
	v_add_f32_e32 v33, v33, v51
	s_mov_b32 s35, s20
	v_mfma_f32_32x32x16_bf16 v[80:95], a[240:243], a[144:147], v[80:95]
	ds_read_b64_tr_b16 v[48:49], v215 offset:0x2600
	v_cvt_pk_bf16_f32 v54, v239, v240
	v_add_f32_e32 v32, v32, v239
	v_add_f32_e32 v33, v33, v240
	s_add_i32 s36, s57, 0x400
	v_mfma_f32_32x32x16_bf16 v[64:79], a[240:243], a[176:179], v[64:79]
	ds_read_b64_tr_b16 v[50:51], v215 offset:0x2e00
	ds_read_b64_tr_b16 v[44:45], v215 offset:0x3000
	v_cvt_pk_bf16_f32 v55, v241, v242
	v_add_f32_e32 v32, v32, v241
	v_add_f32_e32 v33, v33, v242
	s_mov_b32 s37, s21
	v_mfma_f32_32x32x16_bf16 v[112:127], a[212:215], a[148:151], v[112:127]
	ds_read_b64_tr_b16 v[46:47], v215 offset:0x3800
	v_add_f32_e32 v32, v32, v227
	v_add_f32_e32 v33, v33, v228
	s_add_i32 s34, s57, 0x800
	s_mov_b32 s38, s34
	v_mfma_f32_32x32x16_bf16 v[96:111], a[212:215], a[180:183], v[96:111]
	ds_read_b64_tr_b16 v[40:41], v215 offset:0x3200
	v_add_f32_e32 v32, v32, v229
	v_add_f32_e32 v33, v33, v230
	s_mov_b32 s39, s22
	v_mfma_f32_32x32x16_bf16 v[80:95], a[244:247], a[148:151], v[80:95]
	ds_read_b64_tr_b16 v[42:43], v215 offset:0x3a00
	v_add_f32_e32 v32, v32, v231
	v_add_f32_e32 v33, v33, v232
	s_add_i32 s40, s57, 0xc00
	v_mfma_f32_32x32x16_bf16 v[64:79], a[244:247], a[180:183], v[64:79]
	ds_read_b64_tr_b16 v[36:37], v215 offset:0x3400
	ds_read_b64_tr_b16 v[38:39], v215 offset:0x3c00
	v_add_f32_e32 v156, v32, v233
	v_add_f32_e32 v157, v33, v234
	s_mov_b32 s41, s23
	v_mfma_f32_32x32x16_bf16 v[112:127], a[216:219], a[152:155], v[112:127]
	ds_read_b64_tr_b16 v[32:33], v215 offset:0x3600
	v_cvt_pk_bf16_f32 v140, v141, v142
	v_add_f32_e32 v158, v237, v141
	v_add_f32_e32 v142, v238, v142
	s_mov_b32 s42, s58
	v_mfma_f32_32x32x16_bf16 v[96:111], a[216:219], a[184:187], v[96:111]
	ds_read_b64_tr_b16 v[34:35], v215 offset:0x3e00
	v_cvt_pk_bf16_f32 v141, v143, v243
	v_add_f32_e32 v143, v158, v143
	v_add_f32_e32 v158, v142, v243
	v_mfma_f32_32x32x16_bf16 v[80:95], a[248:251], a[152:155], v[80:95]
	s_mov_b32 s43, s24
	v_cvt_pk_bf16_f32 v142, v244, v245
	v_add_f32_e32 v159, v143, v244
	v_add_f32_e32 v158, v158, v245
	v_mfma_f32_32x32x16_bf16 v[64:79], a[248:251], a[184:187], v[64:79]
	s_add_i32 s44, s58, 0x80
	v_cvt_pk_bf16_f32 v143, v246, v247
	v_add_f32_e32 v159, v159, v246
	v_add_f32_e32 v158, v158, v247
	v_mfma_f32_32x32x16_bf16 v[112:127], a[220:223], a[156:159], v[112:127]
	s_mov_b32 s45, s25
	v_add_f32_e32 v159, v159, v148
	v_add_f32_e32 v158, v158, v149
	v_mfma_f32_32x32x16_bf16 v[96:111], a[220:223], a[188:191], v[96:111]
	s_add_i32 s46, s58, 0x800
	v_add_f32_e32 v159, v159, v150
	v_add_f32_e32 v158, v158, v151
	v_mfma_f32_32x32x16_bf16 v[80:95], a[252:255], a[156:159], v[80:95]
	s_mov_b32 s47, s26
	v_add_f32_e32 v159, v159, v152
	v_add_f32_e32 v158, v158, v153
	v_mfma_f32_32x32x16_bf16 v[64:79], a[252:255], a[188:191], v[64:79]
	s_add_i32 s48, s58, 0x880
	v_add_f32_e32 v159, v159, v154
	v_add_f32_e32 v158, v158, v155
	v_add_f32_e32 v156, v156, v157
	s_waitcnt vmcnt(0) lgkmcnt(0)
	s_barrier
	v_mfma_f32_32x32x16_bf16 a[0:15], v[172:175], v[164:167], a[0:15]
	v_mov_b32_e32 v157, v156
	s_mov_b32 m0, s0
	s_nop 0
	buffer_load_dwordx4 v222, s[12:15], s1 offen lds
	v_mfma_f32_32x32x16_bf16 a[16:31], v[172:175], v[192:195], a[16:31]
	v_permlane32_swap_b32_e32 v156, v157
	v_add_f32_e32 v156, v156, v157
	s_mov_b32 m0, s35
	s_nop 0
	buffer_load_dwordx4 v223, s[12:15], s36 offen lds
	ds_read_b128 a[192:195], v217 offset:0
	v_mfma_f32_32x32x16_bf16 a[32:47], v[184:187], v[164:167], a[32:47]
	v_add_f32_e32 v225, v225, v156
	v_add_f32_e32 v156, v159, v158
	v_mov_b32_e32 v157, v156
	s_mov_b32 m0, s37
	s_nop 0
	buffer_load_dwordx4 v222, s[12:15], s38 offen lds
	ds_read_b128 a[196:199], v199 offset:0
	v_mfma_f32_32x32x16_bf16 a[48:63], v[184:187], v[192:195], a[48:63]
	v_permlane32_swap_b32_e32 v156, v157
	v_add_f32_e32 v156, v156, v157
	s_mov_b32 m0, s39
	s_nop 0
	buffer_load_dwordx4 v223, s[12:15], s40 offen lds
	ds_read_b128 a[200:203], v198 offset:0
	v_mfma_f32_32x32x16_bf16 a[64:79], v[180:183], v[164:167], a[64:79]
	v_add_f32_e32 v226, v226, v156
	s_mov_b32 m0, s41
	s_nop 0
	buffer_load_dwordx4 v196, s[4:7], s42 offen lds
	ds_read_b128 a[204:207], v197 offset:0
	v_mfma_f32_32x32x16_bf16 a[80:95], v[180:183], v[192:195], a[80:95]
	s_mov_b32 m0, s43
	s_nop 0
	buffer_load_dwordx4 v196, s[4:7], s44 offen lds
	ds_read_b128 a[208:211], v217 offset:128
	v_mfma_f32_32x32x16_bf16 a[96:111], v[188:191], v[164:167], a[96:111]
	s_mov_b32 m0, s45
	s_nop 0
	buffer_load_dwordx4 v196, s[4:7], s46 offen lds
	ds_read_b128 a[212:215], v199 offset:128
	v_mfma_f32_32x32x16_bf16 a[112:127], v[188:191], v[192:195], a[112:127]
	s_mov_b32 m0, s47
	s_nop 0
	buffer_load_dwordx4 v196, s[4:7], s48 offen lds
	ds_read_b128 a[216:219], v198 offset:128
	s_nop 0
	v_mfma_f32_32x32x16_bf16 a[0:15], v[176:179], v[128:131], a[0:15]
	ds_read_b128 a[220:223], v197 offset:128
	s_cmp_gt_u32 s27, 12
	s_cbranch_scc1 .Lka_done
	s_cmp_gt_u32 s27, 4
	s_cbranch_scc1 .Lka_single
	v_cvt_pk_bf16_f32 v248, v248, v249
	v_cvt_pk_bf16_f32 v249, v250, v251
	v_cvt_pk_bf16_f32 v250, v252, v253
	v_cvt_pk_bf16_f32 v251, v254, v255
	v_lshrrev_b32_e32 v252, 1, v208
	buffer_store_dwordx4 v[248:251], v252, s[12:15], s56 offen sc1
	v_mbcnt_lo_u32_b32 v253, -1, 0
	v_mbcnt_hi_u32_b32 v253, -1, v253
	v_lshlrev_b32_e32 v253, 4, v253
	v_add_u32_e32 v253, s84, v253
	ds_read_b128 v[248:251], v253
	ds_read_b128 v[252:255], v253 offset:1024
	s_cmp_eq_u32 s27, 2
	s_cbranch_scc0 .Lka_nopub
	s_cmp_eq_u32 s50, 0
	s_cbranch_scc0 .Lf1_pub_done
	v_mov_b32_e32 v210, s70
	s_mov_b64 exec, 1
	global_store_dword v209, v210, s[72:73] offset:3072 sc1
	s_mov_b64 exec, -1
.Lf1_pub_done:
.Lka_nopub:
	s_cmp_eq_u32 s27, 4
	s_cbranch_scc0 .Lka_done
	s_mov_b32 s53, 0x10000
.Lf1_chk:
	v_cmp_ne_u32_e32 vcc, s70, v210
	s_cmp_lg_u64 vcc, 0
	s_cbranch_scc0 .Lf1_ok
	s_sleep 8
	global_load_dword v210, v209, s[64:65] offset:3072 sc1
	s_waitcnt vmcnt(0)
	s_add_i32 s53, s53, -1
	s_cmp_eq_u32 s53, 0
	s_cbranch_scc0 .Lf1_chk
.Lf1_ok:
	s_branch .Lka_done
.Lka_single:
	v_cvt_pk_bf16_f32 v248, v248, v249
	v_cvt_pk_bf16_f32 v249, v250, v251
	v_cvt_pk_bf16_f32 v250, v252, v253
	v_cvt_pk_bf16_f32 v251, v254, v255
	v_lshrrev_b32_e32 v252, 1, v208
	buffer_store_dwordx4 v[248:251], v252, s[12:15], s56 offen sc1
	s_nop 1
	global_load_dwordx4 v[248:251], v208, s[74:75] nt
	global_load_dwordx4 v[252:255], v208, s[74:75] offset:16 nt
	s_add_u32 s74, s74, 0x2000
	s_addc_u32 s75, s75, 0
.Lka_done:
	v_max3_f32 v156, v112, v113, v80
	v_max3_f32 v157, v114, v115, v81
	s_nop 0
	v_max3_f32 v156, v156, v82, v83
	v_mfma_f32_32x32x16_bf16 a[16:31], v[176:179], v[144:147], a[16:31]
	ds_read_b128 a[224:227], v217 offset:8192
	v_max3_f32 v156, v156, v116, v117
	v_max3_f32 v157, v157, v118, v119
	v_max3_f32 v156, v156, v84, v85
	v_max3_f32 v157, v157, v86, v87
	v_mfma_f32_32x32x16_bf16 a[32:47], v[168:171], v[128:131], a[32:47]
	ds_read_b128 a[228:231], v199 offset:8192
	v_max3_f32 v156, v156, v120, v121
	v_max3_f32 v157, v157, v122, v123
	v_max3_f32 v156, v156, v88, v89
	v_max3_f32 v157, v157, v90, v91
	v_mfma_f32_32x32x16_bf16 a[48:63], v[168:171], v[144:147], a[48:63]
	ds_read_b128 a[232:235], v198 offset:8192
	v_max3_f32 v156, v156, v124, v125
	v_max3_f32 v157, v157, v126, v127
	v_max3_f32 v156, v156, v92, v93
	v_max3_f32 v157, v157, v94, v95
	v_mfma_f32_32x32x16_bf16 a[64:79], v[160:163], v[128:131], a[64:79]
	ds_read_b128 a[236:239], v197 offset:8192
	v_max3_f32 v158, v96, v97, v64
	v_max3_f32 v159, v98, v99, v65
	v_max3_f32 v158, v158, v66, v67
	v_mfma_f32_32x32x16_bf16 a[80:95], v[160:163], v[144:147], a[80:95]
	ds_read_b128 a[240:243], v217 offset:8320
	v_max3_f32 v158, v158, v100, v101
	v_max3_f32 v159, v159, v102, v103
	v_max3_f32 v158, v158, v68, v69
	v_max3_f32 v159, v159, v70, v71
	v_mfma_f32_32x32x16_bf16 a[96:111], v[136:139], v[128:131], a[96:111]
	ds_read_b128 a[244:247], v199 offset:8320
	v_max3_f32 v128, v158, v104, v105
	v_max3_f32 v129, v159, v106, v107
	v_max3_f32 v128, v128, v72, v73
	v_max3_f32 v129, v129, v74, v75
	v_mfma_f32_32x32x16_bf16 a[112:127], v[136:139], v[144:147], a[112:127]
	ds_read_b128 a[248:251], v198 offset:8320
	v_max3_f32 v128, v128, v108, v109
	v_max3_f32 v129, v129, v110, v111
	v_max3_f32 v128, v128, v76, v77
	v_max3_f32 v130, v129, v78, v79
	v_mfma_f32_32x32x16_bf16 a[0:15], v[132:135], v[52:55], a[0:15]
	ds_read_b128 a[252:255], v197 offset:8320
	s_cmp_gt_u32 s27, 4
	s_cbranch_scc1 .Lkb2_done
	s_waitcnt lgkmcnt(8)
	v_pk_add_f32 v[200:201], v[248:249], v[200:201]
	v_pk_add_f32 v[202:203], v[250:251], v[202:203]
	v_pk_add_f32 v[204:205], v[252:253], v[204:205]
	v_pk_add_f32 v[206:207], v[254:255], v[206:207]
	v_cvt_pk_bf16_f32 v248, v248, v249
	v_cvt_pk_bf16_f32 v249, v250, v251
	v_cvt_pk_bf16_f32 v250, v252, v253
	v_cvt_pk_bf16_f32 v251, v254, v255
	v_lshrrev_b32_e32 v252, 1, v208
	buffer_store_dwordx4 v[248:251], v252, s[4:7], s56 offen sc1
	s_add_i32 s56, s56, 0x1000
	s_nop 1
	global_load_dwordx4 v[248:251], v208, s[54:55] nt
	global_load_dwordx4 v[252:255], v208, s[54:55] offset:16 nt
	s_add_u32 s54, s54, 0x2000
	s_addc_u32 s55, s55, 0
	s_mov_b32 m0, s84
	s_nop 0
	buffer_load_dwordx4 v208, s[80:83], s86 offen lds
	s_mov_b32 m0, s85
	s_nop 0
	buffer_load_dwordx4 v208, s[80:83], s86 offen offset:16 lds
	s_add_i32 s86, s86, 0x2000
.Lkb2_done:
	v_max_f32_e32 v129, v156, v157
	s_nop 0
	v_mov_b32_e32 v131, v129
	s_nop 1
	v_permlane32_swap_b32_e32 v129, v131
	v_max_f32_e32 v129, v129, v131
	v_mfma_f32_32x32x16_bf16 a[16:31], v[132:135], v[140:143], a[16:31]
	v_max_f32_e32 v128, v128, v130
	v_mov_b32_e32 v130, v128
	s_nop 1
	v_permlane32_swap_b32_e32 v128, v130
	v_max_f32_e32 v128, v128, v130
	v_max_f32_e32 v130, v129, v129
	v_max_f32_e32 v131, v128, v128
	v_max_f32_e32 v130, v130, v131
	v_mfma_f32_32x32x16_bf16 a[32:47], v[60:63], v[52:55], a[32:47]
	v_cmp_lt_f32_e32 vcc, s31, v130
	s_cmp_lg_u64 vcc, 0
	s_cselect_b64 s[0:1], -1, 0
	s_cbranch_vccnz .LBB0_22

.LBB0_19:
	s_waitcnt lgkmcnt(0)
	v_mfma_f32_32x32x16_bf16 v[112:127], a[192:195], a[128:131], v[0:15]
	v_exp_f32_e32 v80, v80
	v_exp_f32_e32 v81, v81
	ds_read_b64_tr_b16 v[180:181], v212 offset:0
	v_cvt_pk_bf16_f32 v168, v128, v129
	v_exp_f32_e32 v82, v82
	v_exp_f32_e32 v83, v83
	v_mfma_f32_32x32x16_bf16 v[96:111], a[192:195], a[160:163], v[16:31]
	ds_read_b64_tr_b16 v[182:183], v212 offset:0x800
	v_cvt_pk_bf16_f32 v169, v130, v131
	v_mfma_f32_32x32x16_bf16 v[48:63], a[224:227], a[128:131], v[0:15]
	ds_read_b64_tr_b16 v[184:185], v212 offset:0x200
	v_exp_f32_e32 v239, v84
	v_exp_f32_e32 v240, v85
	v_cvt_pk_bf16_f32 v170, v132, v133
	v_mfma_f32_32x32x16_bf16 v[32:47], a[224:227], a[160:163], v[16:31]
	ds_read_b64_tr_b16 v[186:187], v212 offset:0xa00
	ds_read_b64_tr_b16 v[176:177], v212 offset:0x400
	v_exp_f32_e32 v241, v86
	v_exp_f32_e32 v242, v87
	v_cvt_pk_bf16_f32 v171, v134, v135
	v_exp_f32_e32 v227, v88
	v_exp_f32_e32 v228, v89
	v_mfma_f32_32x32x16_bf16 v[112:127], a[196:199], a[132:135], v[112:127]
	ds_read_b64_tr_b16 v[178:179], v212 offset:0xc00
	v_cvt_pk_bf16_f32 v128, v136, v137
	v_exp_f32_e32 v229, v90
	v_exp_f32_e32 v230, v91
	v_mfma_f32_32x32x16_bf16 v[96:111], a[196:199], a[164:167], v[96:111]
	ds_read_b64_tr_b16 v[188:189], v212 offset:0x600
	v_cvt_pk_bf16_f32 v129, v138, v139
	v_exp_f32_e32 v231, v92
	v_exp_f32_e32 v232, v93
	v_mfma_f32_32x32x16_bf16 v[48:63], a[228:231], a[132:135], v[48:63]
	ds_read_b64_tr_b16 v[190:191], v212 offset:0xe00
	v_cvt_pk_bf16_f32 v130, v140, v141
	v_mfma_f32_32x32x16_bf16 v[32:47], a[228:231], a[164:167], v[32:47]
	ds_read_b64_tr_b16 v[172:173], v212 offset:0x1000
	v_exp_f32_e32 v233, v94
	v_exp_f32_e32 v234, v95
	ds_read_b64_tr_b16 v[174:175], v212 offset:0x1800
	v_cvt_pk_bf16_f32 v131, v142, v143
	v_exp_f32_e32 v141, v64
	v_exp_f32_e32 v142, v65
	v_mfma_f32_32x32x16_bf16 v[112:127], a[200:203], a[136:139], v[112:127]
	ds_read_b64_tr_b16 v[164:165], v212 offset:0x1200
	v_cvt_pk_bf16_f32 v192, v144, v145
	v_exp_f32_e32 v143, v66
	v_mfma_f32_32x32x16_bf16 v[96:111], a[200:203], a[168:171], v[96:111]
	ds_read_b64_tr_b16 v[166:167], v212 offset:0x1a00
	v_exp_f32_e32 v243, v67
	v_cvt_pk_bf16_f32 v193, v146, v147
	v_mfma_f32_32x32x16_bf16 v[48:63], a[232:235], a[136:139], v[48:63]
	ds_read_b64_tr_b16 v[160:161], v212 offset:0x1400
	v_exp_f32_e32 v244, v68
	v_exp_f32_e32 v245, v69
	v_cvt_pk_bf16_f32 v194, v148, v149
	v_mfma_f32_32x32x16_bf16 v[32:47], a[232:235], a[168:171], v[32:47]
	ds_read_b64_tr_b16 v[162:163], v212 offset:0x1c00
	ds_read_b64_tr_b16 v[136:137], v212 offset:0x1600
	v_exp_f32_e32 v246, v70
	v_exp_f32_e32 v247, v71
	v_cvt_pk_bf16_f32 v195, v150, v151
	v_exp_f32_e32 v148, v72
	v_exp_f32_e32 v149, v73
	v_mfma_f32_32x32x16_bf16 v[112:127], a[204:207], a[140:143], v[112:127]
	ds_read_b64_tr_b16 v[138:139], v212 offset:0x1e00
	v_cvt_pk_bf16_f32 v144, v152, v153
	v_exp_f32_e32 v150, v74
	v_exp_f32_e32 v151, v75
	v_mfma_f32_32x32x16_bf16 v[96:111], a[204:207], a[172:175], v[96:111]
	ds_read_b64_tr_b16 v[132:133], v212 offset:0x2000
	v_cvt_pk_bf16_f32 v145, v154, v155
	v_exp_f32_e32 v152, v76
	v_exp_f32_e32 v153, v77
	v_mfma_f32_32x32x16_bf16 v[48:63], a[236:239], a[140:143], v[48:63]
	ds_read_b64_tr_b16 v[134:135], v212 offset:0x2800
	v_cvt_pk_bf16_f32 v146, v156, v157
	v_mfma_f32_32x32x16_bf16 v[32:47], a[236:239], a[172:175], v[32:47]
	ds_read_b64_tr_b16 v[92:93], v212 offset:0x2200
	v_exp_f32_e32 v154, v78
	v_exp_f32_e32 v155, v79
	ds_read_b64_tr_b16 v[94:95], v212 offset:0x2a00
	v_cvt_pk_bf16_f32 v147, v158, v159
	s_mov_b32 s0, s3
	v_mfma_f32_32x32x16_bf16 v[112:127], a[208:211], a[144:147], v[112:127]
	ds_read_b64_tr_b16 v[88:89], v212 offset:0x2400
	v_cvt_pk_bf16_f32 v84, v80, v81
	v_add_f32_e32 v64, v236, v80
	v_add_f32_e32 v65, v235, v81
	s_add_i32 s58, s57, s60
	s_and_b32 s58, s58, 0x7ffff
	s_mov_b32 s1, s58
	v_mfma_f32_32x32x16_bf16 v[96:111], a[208:211], a[176:179], v[96:111]
	ds_read_b64_tr_b16 v[90:91], v212 offset:0x2c00
	v_cvt_pk_bf16_f32 v85, v82, v83
	v_add_f32_e32 v64, v64, v82
	v_add_f32_e32 v65, v65, v83
	s_mov_b32 s35, s10
	v_mfma_f32_32x32x16_bf16 v[48:63], a[240:243], a[144:147], v[48:63]
	ds_read_b64_tr_b16 v[80:81], v212 offset:0x2600
	v_cvt_pk_bf16_f32 v86, v239, v240
	v_add_f32_e32 v64, v64, v239
	v_add_f32_e32 v65, v65, v240
	s_add_i32 s36, s58, 0x400
	v_mfma_f32_32x32x16_bf16 v[32:47], a[240:243], a[176:179], v[32:47]
	ds_read_b64_tr_b16 v[82:83], v212 offset:0x2e00
	ds_read_b64_tr_b16 v[76:77], v212 offset:0x3000
	v_cvt_pk_bf16_f32 v87, v241, v242
	v_add_f32_e32 v64, v64, v241
	v_add_f32_e32 v65, v65, v242
	s_mov_b32 s37, s11
	v_mfma_f32_32x32x16_bf16 v[112:127], a[212:215], a[148:151], v[112:127]
	ds_read_b64_tr_b16 v[78:79], v212 offset:0x3800
	v_add_f32_e32 v64, v64, v227
	v_add_f32_e32 v65, v65, v228
	s_add_i32 s38, s58, 0x800
	v_mfma_f32_32x32x16_bf16 v[96:111], a[212:215], a[180:183], v[96:111]
	ds_read_b64_tr_b16 v[72:73], v212 offset:0x3200
	v_add_f32_e32 v64, v64, v229
	v_add_f32_e32 v65, v65, v230
	s_mov_b32 s39, s16
	v_mfma_f32_32x32x16_bf16 v[48:63], a[244:247], a[148:151], v[48:63]
	ds_read_b64_tr_b16 v[74:75], v212 offset:0x3a00
	v_add_f32_e32 v64, v64, v231
	v_add_f32_e32 v65, v65, v232
	s_add_i32 s40, s58, 0xc00
	v_mfma_f32_32x32x16_bf16 v[32:47], a[244:247], a[180:183], v[32:47]
	ds_read_b64_tr_b16 v[68:69], v212 offset:0x3400
	ds_read_b64_tr_b16 v[70:71], v212 offset:0x3c00
	v_add_f32_e32 v156, v64, v233
	v_add_f32_e32 v157, v65, v234
	s_mov_b32 s41, s2
	v_mfma_f32_32x32x16_bf16 v[112:127], a[216:219], a[152:155], v[112:127]
	ds_read_b64_tr_b16 v[64:65], v212 offset:0x3600
	v_cvt_pk_bf16_f32 v140, v141, v142
	v_add_f32_e32 v158, v237, v141
	v_add_f32_e32 v142, v238, v142
	v_mfma_f32_32x32x16_bf16 v[96:111], a[216:219], a[184:187], v[96:111]
	ds_read_b64_tr_b16 v[66:67], v212 offset:0x3e00
	v_cvt_pk_bf16_f32 v141, v143, v243
	v_add_f32_e32 v143, v158, v143
	v_add_f32_e32 v158, v142, v243
	v_mfma_f32_32x32x16_bf16 v[48:63], a[248:251], a[152:155], v[48:63]
	s_mov_b32 s42, s17
	v_cvt_pk_bf16_f32 v142, v244, v245
	v_add_f32_e32 v159, v143, v244
	v_add_f32_e32 v158, v158, v245
	v_mfma_f32_32x32x16_bf16 v[32:47], a[248:251], a[184:187], v[32:47]
	s_add_i32 s43, s57, 0x80
	v_cvt_pk_bf16_f32 v143, v246, v247
	v_add_f32_e32 v159, v159, v246
	v_add_f32_e32 v158, v158, v247
	v_mfma_f32_32x32x16_bf16 v[112:127], a[220:223], a[156:159], v[112:127]
	s_mov_b32 s44, s18
	v_add_f32_e32 v159, v159, v148
	v_add_f32_e32 v158, v158, v149
	v_mfma_f32_32x32x16_bf16 v[96:111], a[220:223], a[188:191], v[96:111]
	v_add_f32_e32 v159, v159, v150
	v_add_f32_e32 v158, v158, v151
	v_mfma_f32_32x32x16_bf16 v[48:63], a[252:255], a[156:159], v[48:63]
	s_mov_b32 s45, s19
	v_add_f32_e32 v159, v159, v152
	v_add_f32_e32 v158, v158, v153
	v_mfma_f32_32x32x16_bf16 v[32:47], a[252:255], a[188:191], v[32:47]
	s_add_i32 s46, s57, 0x880
	v_add_f32_e32 v159, v159, v154
	v_add_f32_e32 v158, v158, v155
	v_add_f32_e32 v156, v156, v157
	s_waitcnt vmcnt(0) lgkmcnt(0)
	s_barrier
	v_mfma_f32_32x32x16_bf16 a[0:15], v[180:183], v[168:171], a[0:15]
	v_mov_b32_e32 v157, v156
	s_mov_b32 m0, s0
	s_nop 0
	buffer_load_dwordx4 v222, s[12:15], s1 offen lds
	v_mfma_f32_32x32x16_bf16 a[16:31], v[180:183], v[192:195], a[16:31]
	v_permlane32_swap_b32_e32 v156, v157
	v_add_f32_e32 v156, v156, v157
	s_mov_b32 m0, s35
	s_nop 0
	buffer_load_dwordx4 v223, s[12:15], s36 offen lds
	ds_read_b128 a[192:195], v218 offset:0
	v_mfma_f32_32x32x16_bf16 a[32:47], v[184:187], v[168:171], a[32:47]
	v_add_f32_e32 v225, v225, v156
	v_add_f32_e32 v156, v159, v158
	v_mov_b32_e32 v157, v156
	s_mov_b32 m0, s37
	s_nop 0
	buffer_load_dwordx4 v222, s[12:15], s38 offen lds
	ds_read_b128 a[196:199], v219 offset:0
	v_mfma_f32_32x32x16_bf16 a[48:63], v[184:187], v[192:195], a[48:63]
	v_permlane32_swap_b32_e32 v156, v157
	v_add_f32_e32 v156, v156, v157
	s_mov_b32 m0, s39
	s_nop 0
	buffer_load_dwordx4 v223, s[12:15], s40 offen lds
	ds_read_b128 a[200:203], v220 offset:0
	v_mfma_f32_32x32x16_bf16 a[64:79], v[176:179], v[168:171], a[64:79]
	v_add_f32_e32 v226, v226, v156
	s_mov_b32 m0, s41
	s_nop 0
	buffer_load_dwordx4 v196, s[4:7], s33 offen lds
	ds_read_b128 a[204:207], v221 offset:0
	v_mfma_f32_32x32x16_bf16 a[80:95], v[176:179], v[192:195], a[80:95]
	s_mov_b32 m0, s42
	s_nop 0
	buffer_load_dwordx4 v196, s[4:7], s43 offen lds
	ds_read_b128 a[208:211], v218 offset:128
	v_mfma_f32_32x32x16_bf16 a[96:111], v[188:191], v[168:171], a[96:111]
	s_mov_b32 m0, s44
	s_nop 0
	buffer_load_dwordx4 v196, s[4:7], s34 offen lds
	ds_read_b128 a[212:215], v219 offset:128
	v_mfma_f32_32x32x16_bf16 a[112:127], v[188:191], v[192:195], a[112:127]
	s_mov_b32 m0, s45
	s_nop 0
	buffer_load_dwordx4 v196, s[4:7], s46 offen lds
	ds_read_b128 a[216:219], v220 offset:128
	s_nop 0
	v_mfma_f32_32x32x16_bf16 a[0:15], v[172:175], v[128:131], a[0:15]
	ds_read_b128 a[220:223], v221 offset:128
	s_cmp_gt_u32 s27, 12
	s_cbranch_scc1 .Lkc_done
	s_cmp_gt_u32 s27, 4
	s_cbranch_scc1 .Lkc_single
	v_cvt_pk_bf16_f32 v248, v248, v249
	v_cvt_pk_bf16_f32 v249, v250, v251
	v_cvt_pk_bf16_f32 v250, v252, v253
	v_cvt_pk_bf16_f32 v251, v254, v255
	v_lshrrev_b32_e32 v252, 1, v208
	buffer_store_dwordx4 v[248:251], v252, s[12:15], s56 offen sc1
	v_mbcnt_lo_u32_b32 v253, -1, 0
	v_mbcnt_hi_u32_b32 v253, -1, v253
	v_lshlrev_b32_e32 v253, 4, v253
	v_add_u32_e32 v253, s84, v253
	ds_read_b128 v[248:251], v253
	ds_read_b128 v[252:255], v253 offset:1024
	s_branch .Lkc_done
.Lkc_single:
	v_pk_add_f32 v[200:201], v[248:249], v[200:201]
	v_pk_add_f32 v[202:203], v[250:251], v[202:203]
	v_pk_add_f32 v[204:205], v[252:253], v[204:205]
	v_pk_add_f32 v[206:207], v[254:255], v[206:207]
	v_cvt_pk_bf16_f32 v248, v248, v249
	v_cvt_pk_bf16_f32 v249, v250, v251
	v_cvt_pk_bf16_f32 v250, v252, v253
	v_cvt_pk_bf16_f32 v251, v254, v255
	v_lshrrev_b32_e32 v252, 1, v208
	buffer_store_dwordx4 v[248:251], v252, s[4:7], s56 offen sc1
	s_add_i32 s56, s56, 0x1000
	s_cmp_gt_u32 s27, 10
	s_cbranch_scc1 .Lkc_done
	s_nop 1
	global_load_dwordx4 v[248:251], v208, s[54:55] nt
	global_load_dwordx4 v[252:255], v208, s[54:55] offset:16 nt
	s_add_u32 s54, s54, 0x2000
	s_addc_u32 s55, s55, 0
.Lkc_done:
	v_max3_f32 v156, v112, v113, v48
	v_max3_f32 v157, v114, v115, v49
	s_nop 0
	v_max3_f32 v156, v156, v50, v51
	v_mfma_f32_32x32x16_bf16 a[16:31], v[172:175], v[144:147], a[16:31]
	ds_read_b128 a[224:227], v218 offset:8192
	v_max3_f32 v156, v156, v116, v117
	v_max3_f32 v157, v157, v118, v119
	v_max3_f32 v156, v156, v52, v53
	v_max3_f32 v157, v157, v54, v55
	v_mfma_f32_32x32x16_bf16 a[32:47], v[164:167], v[128:131], a[32:47]
	ds_read_b128 a[228:231], v219 offset:8192
	v_max3_f32 v156, v156, v120, v121
	v_max3_f32 v157, v157, v122, v123
	v_max3_f32 v156, v156, v56, v57
	v_max3_f32 v157, v157, v58, v59
	v_mfma_f32_32x32x16_bf16 a[48:63], v[164:167], v[144:147], a[48:63]
	ds_read_b128 a[232:235], v220 offset:8192
	v_max3_f32 v156, v156, v124, v125
	v_max3_f32 v157, v157, v126, v127
	v_max3_f32 v156, v156, v60, v61
	v_max3_f32 v157, v157, v62, v63
	v_mfma_f32_32x32x16_bf16 a[64:79], v[160:163], v[128:131], a[64:79]
	ds_read_b128 a[236:239], v221 offset:8192
	v_max3_f32 v158, v96, v97, v32
	v_max3_f32 v159, v98, v99, v33
	v_max3_f32 v158, v158, v34, v35
	v_mfma_f32_32x32x16_bf16 a[80:95], v[160:163], v[144:147], a[80:95]
	ds_read_b128 a[240:243], v218 offset:8320
	v_max3_f32 v158, v158, v100, v101
	v_max3_f32 v159, v159, v102, v103
	v_max3_f32 v158, v158, v36, v37
	v_max3_f32 v159, v159, v38, v39
	v_mfma_f32_32x32x16_bf16 a[96:111], v[136:139], v[128:131], a[96:111]
	ds_read_b128 a[244:247], v219 offset:8320
	v_max3_f32 v128, v158, v104, v105
	v_max3_f32 v129, v159, v106, v107
	v_max3_f32 v128, v128, v40, v41
	v_max3_f32 v129, v129, v42, v43
	v_mfma_f32_32x32x16_bf16 a[112:127], v[136:139], v[144:147], a[112:127]
	ds_read_b128 a[248:251], v220 offset:8320
	v_max3_f32 v128, v128, v108, v109
	v_max3_f32 v129, v129, v110, v111
	v_max3_f32 v128, v128, v44, v45
	v_max3_f32 v130, v129, v46, v47
	v_mfma_f32_32x32x16_bf16 a[0:15], v[132:135], v[84:87], a[0:15]
	ds_read_b128 a[252:255], v221 offset:8320
	s_cmp_gt_u32 s27, 4
	s_cbranch_scc1 .Lkd2_done
	s_waitcnt lgkmcnt(8)
	v_pk_add_f32 v[200:201], v[248:249], v[200:201]
	v_pk_add_f32 v[202:203], v[250:251], v[202:203]
	v_pk_add_f32 v[204:205], v[252:253], v[204:205]
	v_pk_add_f32 v[206:207], v[254:255], v[206:207]
	v_cvt_pk_bf16_f32 v248, v248, v249
	v_cvt_pk_bf16_f32 v249, v250, v251
	v_cvt_pk_bf16_f32 v250, v252, v253
	v_cvt_pk_bf16_f32 v251, v254, v255
	v_lshrrev_b32_e32 v252, 1, v208
	buffer_store_dwordx4 v[248:251], v252, s[4:7], s56 offen sc1
	s_add_i32 s56, s56, 0x1000
	s_nop 1
	global_load_dwordx4 v[248:251], v208, s[54:55] nt
	global_load_dwordx4 v[252:255], v208, s[54:55] offset:16 nt
	s_add_u32 s54, s54, 0x2000
	s_addc_u32 s55, s55, 0
	s_cmp_gt_u32 s27, 2
	s_cbranch_scc1 .Lkd2_done
	s_mov_b32 m0, s84
	s_nop 0
	buffer_load_dwordx4 v208, s[80:83], s86 offen lds
	s_mov_b32 m0, s85
	s_nop 0
	buffer_load_dwordx4 v208, s[80:83], s86 offen offset:16 lds
	s_add_i32 s86, s86, 0x2000
.Lkd2_done:
	v_max_f32_e32 v129, v156, v157
	s_nop 0
	v_mov_b32_e32 v131, v129
	s_nop 1
	v_permlane32_swap_b32_e32 v129, v131
	v_max_f32_e32 v129, v129, v131
	v_mfma_f32_32x32x16_bf16 a[16:31], v[132:135], v[140:143], a[16:31]
	v_max_f32_e32 v128, v128, v130
	v_mov_b32_e32 v130, v128
	s_nop 1
	v_permlane32_swap_b32_e32 v128, v130
	v_max_f32_e32 v128, v128, v130
	v_max_f32_e32 v130, v129, v129
	v_max_f32_e32 v131, v128, v128
	v_max_f32_e32 v130, v130, v131
	v_mfma_f32_32x32x16_bf16 a[32:47], v[92:95], v[84:87], a[32:47]
	v_cmp_lt_f32_e32 vcc, s31, v130
	s_cmp_lg_u64 vcc, 0
	s_cselect_b64 s[0:1], -1, 0
	s_cbranch_vccnz .LBB0_24

.LBB0_21:
	s_waitcnt lgkmcnt(0)
	s_add_i32 s27, s27, 2
	s_mov_b32 s59, s66
	s_bitcmp1_b32 s71, s27
	s_cbranch_scc1 .Ltail_events

.Ltail_events:
	s_cmp_eq_u32 s27, 4
	s_cbranch_scc1 .Ltail_smp1
	s_cmp_eq_u32 s27, 8
	s_cbranch_scc1 .Ltail_pub2
	s_cmp_eq_u32 s27, 10
	s_cbranch_scc1 .Ltail_smp2
	s_cmp_eq_u32 s27, 14
	s_cbranch_scc1 .Ltail_cs
	s_cmp_eq_u32 s27, 16
	s_cbranch_scc1 .Ltail_pub3
	s_cmp_eq_u32 s27, 18
	s_cbranch_scc1 .Ltail_smp3
	s_mov_b32 s59, s69
	s_mov_b32 s53, 0x10000
	s_cmp_eq_u32 s27, 12
	s_cbranch_scc0 .Ltail_chk3

.Ltail_smp1:
	s_mov_b32 s59, s69
	global_load_dword v210, v209, s[64:65] offset:3072 sc1
	s_branch .Ltail_resume

.LBB0_36:
	s_lshl_b32 s53, s50, 6
	s_add_i32 s53, s53, s52
	v_mov_b32_e32 v200, s53
	s_lshl_b32 s53, s50, 14
	s_add_i32 s53, s53, 0x10000
	v_mov_b32_e32 v201, s53
	v_mbcnt_lo_u32_b32 v204, -1, 0
	v_mbcnt_hi_u32_b32 v204, -1, v204
	v_lshrrev_b32_e32 v202, 4, v204
	v_add_u32_e32 v203, 4, v202
	v_add_u32_e32 v205, 8, v202
	v_add_u32_e32 v206, 12, v202
	v_add_u32_e32 v207, 16, v202
	v_add_u32_e32 v208, 20, v202
	v_add_u32_e32 v209, 24, v202
	v_add_u32_e32 v210, 28, v202
	v_mfma_f32_32x32x16_bf16 v[112:127], a[192:195], a[128:131], v[0:15]
	v_exp_f32_e32 v48, v48
	v_exp_f32_e32 v49, v49
	ds_read_b64_tr_b16 v[180:181], v215 offset:0
	v_cvt_pk_bf16_f32 v164, v128, v129
	v_exp_f32_e32 v50, v50
	v_exp_f32_e32 v51, v51
	v_mfma_f32_32x32x16_bf16 v[96:111], a[192:195], a[160:163], v[16:31]
	ds_read_b64_tr_b16 v[182:183], v215 offset:0x800
	v_cvt_pk_bf16_f32 v165, v130, v131
	v_mfma_f32_32x32x16_bf16 v[80:95], a[224:227], a[128:131], v[0:15]
	v_exp_f32_e32 v218, v52
	v_exp_f32_e32 v219, v53
	ds_read_b64_tr_b16 v[188:189], v215 offset:0x200
	v_cvt_pk_bf16_f32 v166, v132, v133
	v_mfma_f32_32x32x16_bf16 v[64:79], a[224:227], a[160:163], v[16:31]
	ds_read_b64_tr_b16 v[190:191], v215 offset:0xa00
	ds_read_b64_tr_b16 v[176:177], v215 offset:0x400
	v_exp_f32_e32 v230, v54
	v_exp_f32_e32 v231, v55
	v_cvt_pk_bf16_f32 v167, v134, v135
	v_exp_f32_e32 v220, v56
	v_exp_f32_e32 v221, v57
	v_mfma_f32_32x32x16_bf16 v[112:127], a[196:199], a[132:135], v[112:127]
	ds_read_b64_tr_b16 v[178:179], v215 offset:0xc00
	v_cvt_pk_bf16_f32 v128, v136, v137
	v_exp_f32_e32 v222, v58
	v_exp_f32_e32 v223, v59
	v_mfma_f32_32x32x16_bf16 v[96:111], a[196:199], a[164:167], v[96:111]
	ds_read_b64_tr_b16 v[184:185], v215 offset:0x600
	v_cvt_pk_bf16_f32 v129, v138, v139
	v_exp_f32_e32 v224, v60
	v_exp_f32_e32 v227, v61
	v_mfma_f32_32x32x16_bf16 v[80:95], a[228:231], a[132:135], v[80:95]
	ds_read_b64_tr_b16 v[186:187], v215 offset:0xe00
	v_cvt_pk_bf16_f32 v130, v140, v141
	v_mfma_f32_32x32x16_bf16 v[64:79], a[228:231], a[164:167], v[64:79]
	ds_read_b64_tr_b16 v[172:173], v215 offset:0x1000
	v_exp_f32_e32 v228, v62
	v_exp_f32_e32 v229, v63
	ds_read_b64_tr_b16 v[174:175], v215 offset:0x1800
	v_cvt_pk_bf16_f32 v131, v142, v143
	v_exp_f32_e32 v141, v32
	v_exp_f32_e32 v142, v33
	v_mfma_f32_32x32x16_bf16 v[112:127], a[200:203], a[136:139], v[112:127]
	ds_read_b64_tr_b16 v[168:169], v215 offset:0x1200
	v_cvt_pk_bf16_f32 v192, v144, v145
	v_exp_f32_e32 v143, v34
	v_mfma_f32_32x32x16_bf16 v[96:111], a[200:203], a[168:171], v[96:111]
	ds_read_b64_tr_b16 v[170:171], v215 offset:0x1a00
	v_exp_f32_e32 v232, v35
	v_cvt_pk_bf16_f32 v193, v146, v147
	v_mfma_f32_32x32x16_bf16 v[80:95], a[232:235], a[136:139], v[80:95]
	ds_read_b64_tr_b16 v[160:161], v215 offset:0x1400
	v_exp_f32_e32 v233, v36
	v_exp_f32_e32 v234, v37
	v_cvt_pk_bf16_f32 v194, v148, v149
	v_mfma_f32_32x32x16_bf16 v[64:79], a[232:235], a[168:171], v[64:79]
	ds_read_b64_tr_b16 v[162:163], v215 offset:0x1c00
	ds_read_b64_tr_b16 v[136:137], v215 offset:0x1600
	v_exp_f32_e32 v239, v38
	v_exp_f32_e32 v240, v39
	v_cvt_pk_bf16_f32 v195, v150, v151
	v_exp_f32_e32 v148, v40
	v_exp_f32_e32 v149, v41
	v_mfma_f32_32x32x16_bf16 v[112:127], a[204:207], a[140:143], v[112:127]
	ds_read_b64_tr_b16 v[138:139], v215 offset:0x1e00
	v_cvt_pk_bf16_f32 v144, v152, v153
	v_exp_f32_e32 v150, v42
	v_exp_f32_e32 v151, v43
	v_mfma_f32_32x32x16_bf16 v[96:111], a[204:207], a[172:175], v[96:111]
	ds_read_b64_tr_b16 v[132:133], v215 offset:0x2000
	v_cvt_pk_bf16_f32 v145, v154, v155
	v_exp_f32_e32 v152, v44
	v_exp_f32_e32 v153, v45
	v_mfma_f32_32x32x16_bf16 v[80:95], a[236:239], a[140:143], v[80:95]
	ds_read_b64_tr_b16 v[134:135], v215 offset:0x2800
	v_cvt_pk_bf16_f32 v146, v156, v157
	v_mfma_f32_32x32x16_bf16 v[64:79], a[236:239], a[172:175], v[64:79]
	ds_read_b64_tr_b16 v[60:61], v215 offset:0x2200
	v_exp_f32_e32 v154, v46
	v_exp_f32_e32 v155, v47
	ds_read_b64_tr_b16 v[62:63], v215 offset:0x2a00
	v_cvt_pk_bf16_f32 v147, v158, v159
	v_mfma_f32_32x32x16_bf16 v[112:127], a[208:211], a[144:147], v[112:127]
	ds_read_b64_tr_b16 v[56:57], v215 offset:0x2400
	v_cvt_pk_bf16_f32 v52, v48, v49
	v_add_f32_e32 v32, v236, v48
	v_add_f32_e32 v33, v235, v49
	s_add_i32 s12, s28, 0x80000
	s_mov_b32 s0, s12
	v_mfma_f32_32x32x16_bf16 v[96:111], a[208:211], a[176:179], v[96:111]
	ds_read_b64_tr_b16 v[58:59], v215 offset:0x2c00
	v_cvt_pk_bf16_f32 v53, v50, v51
	v_add_f32_e32 v32, v32, v50
	v_add_f32_e32 v33, v33, v51
	v_mfma_f32_32x32x16_bf16 v[80:95], a[240:243], a[144:147], v[80:95]
	ds_read_b64_tr_b16 v[48:49], v215 offset:0x2600
	v_cvt_pk_bf16_f32 v54, v218, v219
	v_add_f32_e32 v32, v32, v218
	v_add_f32_e32 v33, v33, v219
	s_add_i32 s1, s28, 0x80400
	v_mfma_f32_32x32x16_bf16 v[64:79], a[240:243], a[176:179], v[64:79]
	ds_read_b64_tr_b16 v[50:51], v215 offset:0x2e00
	ds_read_b64_tr_b16 v[44:45], v215 offset:0x3000
	v_cvt_pk_bf16_f32 v55, v230, v231
	v_add_f32_e32 v32, v32, v230
	v_add_f32_e32 v33, v33, v231
	v_mfma_f32_32x32x16_bf16 v[112:127], a[212:215], a[148:151], v[112:127]
	ds_read_b64_tr_b16 v[46:47], v215 offset:0x3800
	v_add_f32_e32 v32, v32, v220
	v_add_f32_e32 v33, v33, v221
	s_add_i32 s13, s28, 0x80800
	s_mov_b32 s14, s13
	v_mfma_f32_32x32x16_bf16 v[96:111], a[212:215], a[180:183], v[96:111]
	ds_read_b64_tr_b16 v[40:41], v215 offset:0x3200
	v_add_f32_e32 v32, v32, v222
	v_add_f32_e32 v33, v33, v223
	v_mfma_f32_32x32x16_bf16 v[80:95], a[244:247], a[148:151], v[80:95]
	ds_read_b64_tr_b16 v[42:43], v215 offset:0x3a00
	v_add_f32_e32 v32, v32, v224
	v_add_f32_e32 v33, v33, v227
	s_add_i32 s15, s28, 0x80c00
	v_mfma_f32_32x32x16_bf16 v[64:79], a[244:247], a[180:183], v[64:79]
	ds_read_b64_tr_b16 v[36:37], v215 offset:0x3400
	ds_read_b64_tr_b16 v[38:39], v215 offset:0x3c00
	v_add_f32_e32 v156, v32, v228
	v_add_f32_e32 v157, v33, v229
	v_mfma_f32_32x32x16_bf16 v[112:127], a[216:219], a[152:155], v[112:127]
	ds_read_b64_tr_b16 v[32:33], v215 offset:0x3600
	v_cvt_pk_bf16_f32 v140, v141, v142
	v_add_f32_e32 v158, v237, v141
	v_add_f32_e32 v142, v238, v142
	s_add_i32 s27, s88, 0x0
	v_mfma_f32_32x32x16_bf16 v[96:111], a[216:219], a[184:187], v[96:111]
	ds_read_b64_tr_b16 v[34:35], v215 offset:0x3e00
	v_cvt_pk_bf16_f32 v141, v143, v232
	v_add_f32_e32 v143, v158, v143
	v_add_f32_e32 v158, v142, v232
	v_mfma_f32_32x32x16_bf16 v[80:95], a[248:251], a[152:155], v[80:95]
	v_cvt_pk_bf16_f32 v142, v233, v234
	v_add_f32_e32 v159, v143, v233
	v_add_f32_e32 v158, v158, v234
	v_mfma_f32_32x32x16_bf16 v[64:79], a[248:251], a[184:187], v[64:79]
	s_add_i32 s30, s88, 0x80
	v_cvt_pk_bf16_f32 v143, v239, v240
	v_add_f32_e32 v159, v159, v239
	v_add_f32_e32 v158, v158, v240
	v_mfma_f32_32x32x16_bf16 v[112:127], a[220:223], a[156:159], v[112:127]
	v_add_f32_e32 v159, v159, v148
	v_add_f32_e32 v158, v158, v149
	v_mfma_f32_32x32x16_bf16 v[96:111], a[220:223], a[188:191], v[96:111]
	s_add_i32 s31, s88, 0x800
	v_add_f32_e32 v159, v159, v150
	v_add_f32_e32 v158, v158, v151
	v_mfma_f32_32x32x16_bf16 v[80:95], a[252:255], a[156:159], v[80:95]
	v_add_f32_e32 v159, v159, v152
	v_add_f32_e32 v158, v158, v153
	v_mfma_f32_32x32x16_bf16 v[64:79], a[252:255], a[188:191], v[64:79]
	s_add_i32 s33, s88, 0x880
	v_add_f32_e32 v159, v159, v154
	v_add_f32_e32 v158, v158, v155
	v_add_f32_e32 v156, v156, v157
	s_waitcnt vmcnt(0) lgkmcnt(0)
	s_barrier
	v_mfma_f32_32x32x16_bf16 a[0:15], v[180:183], v[164:167], a[0:15]
	v_mov_b32_e32 v157, v156
	v_mfma_f32_32x32x16_bf16 a[16:31], v[180:183], v[192:195], a[16:31]
	s_nop 1
	v_permlane32_swap_b32_e32 v156, v157
	v_add_f32_e32 v156, v156, v157
	ds_read_b128 a[192:195], v217 offset:0
	v_mfma_f32_32x32x16_bf16 a[32:47], v[188:191], v[164:167], a[32:47]
	v_add_f32_e32 v219, v225, v156
	v_add_f32_e32 v156, v159, v158
	v_mov_b32_e32 v157, v156
	ds_read_b128 a[196:199], v199 offset:0
	v_mfma_f32_32x32x16_bf16 a[48:63], v[188:191], v[192:195], a[48:63]
	v_permlane32_swap_b32_e32 v156, v157
	v_add_f32_e32 v156, v156, v157
	ds_read_b128 a[200:203], v198 offset:0
	v_mfma_f32_32x32x16_bf16 a[64:79], v[176:179], v[164:167], a[64:79]
	v_add_f32_e32 v218, v226, v156
	s_mov_b32 m0, s23
	s_nop 0
	buffer_load_dwordx4 v196, s[4:7], s27 offen lds
	ds_read_b128 a[204:207], v197 offset:0
	v_mfma_f32_32x32x16_bf16 a[80:95], v[176:179], v[192:195], a[80:95]
	s_mov_b32 m0, s24
	s_nop 0
	buffer_load_dwordx4 v196, s[4:7], s30 offen lds
	ds_read_b128 a[208:211], v217 offset:128
	v_mfma_f32_32x32x16_bf16 a[96:111], v[184:187], v[164:167], a[96:111]
	s_mov_b32 m0, s25
	s_nop 0
	buffer_load_dwordx4 v196, s[4:7], s31 offen lds
	ds_read_b128 a[212:215], v199 offset:128
	v_mfma_f32_32x32x16_bf16 a[112:127], v[184:187], v[192:195], a[112:127]
	s_mov_b32 m0, s26
	s_nop 0
	buffer_load_dwordx4 v196, s[4:7], s33 offen lds
	ds_read_b128 a[216:219], v198 offset:128
	v_mfma_f32_32x32x16_bf16 a[0:15], v[172:175], v[128:131], a[0:15]
	ds_read_b128 a[220:223], v197 offset:128
	v_max3_f32 v156, v112, v113, v80
	v_max3_f32 v157, v114, v115, v81
	v_max3_f32 v156, v156, v82, v83
	v_mfma_f32_32x32x16_bf16 a[16:31], v[172:175], v[144:147], a[16:31]
	ds_read_b128 a[224:227], v217 offset:8192
	v_max3_f32 v156, v156, v116, v117
	v_max3_f32 v157, v157, v118, v119
	v_max3_f32 v156, v156, v84, v85
	v_max3_f32 v157, v157, v86, v87
	v_mfma_f32_32x32x16_bf16 a[32:47], v[168:171], v[128:131], a[32:47]
	ds_read_b128 a[228:231], v199 offset:8192
	v_max3_f32 v156, v156, v120, v121
	v_max3_f32 v157, v157, v122, v123
	v_max3_f32 v156, v156, v88, v89
	v_max3_f32 v157, v157, v90, v91
	v_mfma_f32_32x32x16_bf16 a[48:63], v[168:171], v[144:147], a[48:63]
	ds_read_b128 a[232:235], v198 offset:8192
	v_max3_f32 v156, v156, v124, v125
	v_max3_f32 v157, v157, v126, v127
	v_max3_f32 v156, v156, v92, v93
	v_max3_f32 v157, v157, v94, v95
	v_mfma_f32_32x32x16_bf16 a[64:79], v[160:163], v[128:131], a[64:79]
	ds_read_b128 a[236:239], v197 offset:8192
	v_max3_f32 v158, v96, v97, v64
	v_max3_f32 v159, v98, v99, v65
	v_max3_f32 v158, v158, v66, v67
	v_mfma_f32_32x32x16_bf16 a[80:95], v[160:163], v[144:147], a[80:95]
	ds_read_b128 a[240:243], v217 offset:8320
	v_max3_f32 v158, v158, v100, v101
	v_max3_f32 v159, v159, v102, v103
	v_max3_f32 v158, v158, v68, v69
	v_max3_f32 v159, v159, v70, v71
	v_mfma_f32_32x32x16_bf16 a[96:111], v[136:139], v[128:131], a[96:111]
	ds_read_b128 a[244:247], v199 offset:8320
	v_max3_f32 v128, v158, v104, v105
	v_max3_f32 v129, v159, v106, v107
	v_max3_f32 v128, v128, v72, v73
	v_max3_f32 v129, v129, v74, v75
	v_mfma_f32_32x32x16_bf16 a[112:127], v[136:139], v[144:147], a[112:127]
	ds_read_b128 a[248:251], v198 offset:8320
	v_max3_f32 v128, v128, v108, v109
	v_max3_f32 v129, v129, v110, v111
	v_max3_f32 v128, v128, v76, v77
	v_max3_f32 v130, v129, v78, v79
	v_mfma_f32_32x32x16_bf16 a[0:15], v[132:135], v[52:55], a[0:15]
	ds_read_b128 a[252:255], v197 offset:8320
	v_max_f32_e32 v129, v156, v157
	v_mov_b32_e32 v131, v129
	s_nop 1
	v_permlane32_swap_b32_e32 v129, v131
	v_max_f32_e32 v129, v129, v131
	v_mfma_f32_32x32x16_bf16 a[16:31], v[132:135], v[140:143], a[16:31]
	v_max_f32_e32 v128, v128, v130
	v_mov_b32_e32 v130, v128
	s_nop 1
	v_permlane32_swap_b32_e32 v128, v130
	v_max_f32_e32 v128, v128, v130
	v_max_f32_e32 v130, v129, v129
	v_max_f32_e32 v131, v128, v128
	v_max_f32_e32 v130, v130, v131
	s_mov_b32 s0, 0x41000000
	v_mfma_f32_32x32x16_bf16 a[32:47], v[60:63], v[52:55], a[32:47]
	v_cmp_lt_f32_e32 vcc, s0, v130
	s_cmp_lg_u64 vcc, 0
	s_cselect_b64 s[0:1], -1, 0
	s_cbranch_vccnz .LBB0_43

	.amdhsa_kernel attn_fwd_pwg4x64
		.amdhsa_group_segment_fixed_size 0
		.amdhsa_private_segment_fixed_size 0
		.amdhsa_kernarg_size 72
		.amdhsa_user_sgpr_count 2
		.amdhsa_user_sgpr_dispatch_ptr 0
		.amdhsa_user_sgpr_queue_ptr 0
		.amdhsa_user_sgpr_kernarg_segment_ptr 1
		.amdhsa_user_sgpr_dispatch_id 0
		.amdhsa_user_sgpr_kernarg_preload_length 0
		.amdhsa_user_sgpr_kernarg_preload_offset 0
		.amdhsa_user_sgpr_private_segment_size 0
		.amdhsa_uses_dynamic_stack 0
		.amdhsa_enable_private_segment 0
		.amdhsa_system_sgpr_workgroup_id_x 1
		.amdhsa_system_sgpr_workgroup_id_y 0
		.amdhsa_system_sgpr_workgroup_id_z 0
		.amdhsa_system_sgpr_workgroup_info 0
		.amdhsa_system_vgpr_workitem_id 0
		.amdhsa_next_free_vgpr 512
		.amdhsa_next_free_sgpr 90
		.amdhsa_accum_offset 256
		.amdhsa_reserve_vcc 1
		.amdhsa_float_round_mode_32 0
		.amdhsa_float_round_mode_16_64 0
		.amdhsa_float_denorm_mode_32 3
		.amdhsa_float_denorm_mode_16_64 3
		.amdhsa_dx10_clamp 1
		.amdhsa_ieee_mode 1
		.amdhsa_fp16_overflow 0
		.amdhsa_tg_split 0
		.amdhsa_exception_fp_ieee_invalid_op 0
		.amdhsa_exception_fp_denorm_src 0
		.amdhsa_exception_fp_ieee_div_zero 0
		.amdhsa_exception_fp_ieee_overflow 0
		.amdhsa_exception_fp_ieee_underflow 0
		.amdhsa_exception_fp_ieee_inexact 0
		.amdhsa_exception_int_div_zero 0
	.end_amdhsa_kernel

_Z14headsum_kernelPKtPKfPjPf:
	s_load_dwordx2 s[4:5], s[0:1], 0x0
	s_mov_b32 s3, 0
	s_cmp_lg_u32 s2, 0
	v_mov_b32_e32 v69, 0
	s_cbranch_scc1 .LBB1_2
	s_load_dwordx2 s[6:7], s[0:1], 0x10
	v_lshlrev_b32_e32 v1, 2, v0
	s_waitcnt lgkmcnt(0)
	global_store_dword v1, v69, s[6:7]
	global_store_dword v1, v69, s[6:7] offset:1024
	global_store_dword v1, v69, s[6:7] offset:2048
	global_store_dword v1, v69, s[6:7] offset:3072

amdhsa.kernels:
  - .agpr_count:     256
    .args:
      - .actual_access:  read_only
        .address_space:  global
        .offset:         0
        .size:           8
        .value_kind:     global_buffer
      - .address_space:  global
        .offset:         8
        .size:           8
        .value_kind:     global_buffer
      - .address_space:  global
        .offset:         16
        .size:           8
        .value_kind:     global_buffer
      - .actual_access:  write_only
        .address_space:  global
        .offset:         24
        .size:           8
        .value_kind:     global_buffer
      - .actual_access:  read_only
        .address_space:  global
        .offset:         32
        .size:           8
        .value_kind:     global_buffer
      - .actual_access:  read_only
        .address_space:  global
        .offset:         40
        .size:           8
        .value_kind:     global_buffer
      - .address_space:  global
        .offset:         48
        .size:           8
        .value_kind:     global_buffer
      - .address_space:  global
        .offset:         56
        .size:           8
        .value_kind:     global_buffer
      - .actual_access:  write_only
        .address_space:  global
        .offset:         64
        .size:           8
        .value_kind:     global_buffer
    .group_segment_fixed_size: 0
    .kernarg_segment_align: 8
    .kernarg_segment_size: 72
    .language:       OpenCL C
    .language_version:
      - 2
      - 0
    .max_flat_workgroup_size: 256
    .name:           attn_fwd_pwg4x64
    .private_segment_fixed_size: 0
    .sgpr_count:     96
    .sgpr_spill_count: 0
    .symbol:         attn_fwd_pwg4x64.kd
    .uniform_work_group_size: 1
    .uses_dynamic_stack: false
    .vgpr_count:     512
    .vgpr_spill_count: 0
    .wavefront_size: 64
  - .agpr_count:     0
    .args:
      - .actual_access:  read_only
        .address_space:  global
        .offset:         0
        .size:           8
        .value_kind:     global_buffer
      - .actual_access:  read_only
        .address_space:  global
        .offset:         8
        .size:           8
        .value_kind:     global_buffer
      - .actual_access:  write_only
        .address_space:  global
        .offset:         16
        .size:           8
        .value_kind:     global_buffer
      - .actual_access:  write_only
        .address_space:  global
        .offset:         24
        .size:           8
        .value_kind:     global_buffer
    .group_segment_fixed_size: 4608
    .kernarg_segment_align: 8
    .kernarg_segment_size: 32
    .language:       OpenCL C
    .language_version:
      - 2
      - 0
    .max_flat_workgroup_size: 256
    .name:           _Z14headsum_kernelPKtPKfPjPf
    .private_segment_fixed_size: 0
    .sgpr_count:     22
    .sgpr_spill_count: 0
    .symbol:         _Z14headsum_kernelPKtPKfPjPf.kd
    .uniform_work_group_size: 1
    .uses_dynamic_stack: false
    .vgpr_count:     152
    .vgpr_spill_count: 0
    .wavefront_size: 64
